# static priority (sec 7.4): waves 4-7 at s_setprio 1 through each GEMM K-loop (up/down/in-proj/out), per-segment priority flips removed
# speedup vs baseline: 1.0026x; 1.0026x over previous
.LBB0_390:
	s_andn2_b64 vcc, exec, s[48:49]
	s_cbranch_vccnz .Lprio_in
	s_setprio 1
.Lprio_in:
	s_add_u32 s1, s42, 0x100
	v_lshl_add_u64 v[142:143], s[40:41], 0, v[130:131]
	s_addc_u32 s24, s43, 0
	s_mov_b32 s25, -2
	s_mov_b64 s[42:43], 0
	s_add_u32 s14, s40, s42
	s_addc_u32 s15, s41, s43
	s_add_u32 s34, s14, 0x100
	s_addc_u32 s35, s15, 0
	s_add_u32 s44, s1, s42
	s_addc_u32 s45, s24, s43
	s_cmpk_eq_i32 s42, 0x700
	s_cselect_b64 vcc, -1, 0
	s_and_b64 s[14:15], vcc, exec
	s_cselect_b32 s15, s55, s35
	s_cselect_b32 s14, s54, s34
	s_cselect_b32 s35, s69, s45
	s_cselect_b32 s34, s68, s44
	s_add_i32 s44, 0, 0x11000
	v_add_u32_e32 v145, s44, v1
	s_add_i32 s45, 0, 0x15000
	ds_read_b128 v[146:149], v145
	ds_read_b128 v[150:153], v145 offset:1024
	ds_read_b128 v[154:157], v145 offset:2048
	ds_read_b128 v[158:161], v145 offset:3072
	v_add_u32_e32 v145, s45, v1
	ds_read_b128 v[162:165], v145
	ds_read_b128 v[166:169], v145 offset:1024
	ds_read_b128 v[170:173], v145 offset:2048
	ds_read_b128 v[174:177], v145 offset:3072
	v_cndmask_b32_e32 v193, v131, v141, vcc
	v_cndmask_b32_e32 v192, v130, v140, vcc
	v_lshl_add_u64 v[220:221], v[142:143], 0, s[42:43]
	v_lshl_add_u64 v[222:223], v[220:221], 0, s[6:7]
	s_add_i32 m0, s28, 0xd000
	ds_read_b128 v[178:181], v144 offset:4096
	ds_read_b128 v[182:185], v144 offset:5120
	ds_read_b128 v[196:199], v144 offset:6144
	ds_read_b128 v[200:203], v144 offset:7168
	ds_read_b128 v[204:207], v144 offset:8192
	ds_read_b128 v[208:211], v144 offset:9216
	ds_read_b128 v[212:215], v144 offset:10240
	ds_read_b128 v[216:219], v144 offset:11264
	global_load_lds_dwordx4 v[222:223], off
	v_lshl_add_u64 v[220:221], v[220:221], 0, s[8:9]
	s_add_i32 m0, s28, 0xf000
	s_nop 0
	global_load_lds_dwordx4 v[220:221], off
	s_waitcnt vmcnt(8)
	s_waitcnt lgkmcnt(0)
	s_barrier
	s_waitcnt lgkmcnt(0)
	v_mfma_f32_16x16x32_bf16 v[126:129], v[146:149], v[178:181], 0
	v_mfma_f32_16x16x32_bf16 v[122:125], v[154:157], v[178:181], 0
	v_mfma_f32_16x16x32_bf16 v[110:113], v[146:149], v[196:199], 0
	v_mfma_f32_16x16x32_bf16 v[106:109], v[154:157], v[196:199], 0
	v_mfma_f32_16x16x32_bf16 v[94:97], v[146:149], v[204:207], 0
	v_mfma_f32_16x16x32_bf16 v[90:93], v[154:157], v[204:207], 0
	v_mfma_f32_16x16x32_bf16 v[78:81], v[146:149], v[212:215], 0
	v_mfma_f32_16x16x32_bf16 v[74:77], v[154:157], v[212:215], 0
	v_mfma_f32_16x16x32_bf16 v[126:129], v[150:153], v[182:185], v[126:129]
	v_mfma_f32_16x16x32_bf16 v[122:125], v[158:161], v[182:185], v[122:125]
	v_mfma_f32_16x16x32_bf16 v[110:113], v[150:153], v[200:203], v[110:113]
	v_mfma_f32_16x16x32_bf16 v[106:109], v[158:161], v[200:203], v[106:109]
	v_mfma_f32_16x16x32_bf16 v[94:97], v[150:153], v[208:211], v[94:97]
	v_mfma_f32_16x16x32_bf16 v[90:93], v[158:161], v[208:211], v[90:93]
	v_mfma_f32_16x16x32_bf16 v[78:81], v[150:153], v[216:219], v[78:81]
	v_mfma_f32_16x16x32_bf16 v[74:77], v[158:161], v[216:219], v[74:77]
	v_mfma_f32_16x16x32_bf16 v[118:121], v[162:165], v[178:181], 0
	v_mfma_f32_16x16x32_bf16 v[114:117], v[170:173], v[178:181], 0
	v_mfma_f32_16x16x32_bf16 v[102:105], v[162:165], v[196:199], 0
	v_mfma_f32_16x16x32_bf16 v[98:101], v[170:173], v[196:199], 0
	v_mfma_f32_16x16x32_bf16 v[86:89], v[162:165], v[204:207], 0
	v_mfma_f32_16x16x32_bf16 v[82:85], v[170:173], v[204:207], 0
	v_mfma_f32_16x16x32_bf16 v[70:73], v[162:165], v[212:215], 0
	v_mfma_f32_16x16x32_bf16 v[66:69], v[170:173], v[212:215], 0
	v_mfma_f32_16x16x32_bf16 v[118:121], v[166:169], v[182:185], v[118:121]
	v_mfma_f32_16x16x32_bf16 v[114:117], v[174:177], v[182:185], v[114:117]
	v_mfma_f32_16x16x32_bf16 v[102:105], v[166:169], v[200:203], v[102:105]
	v_mfma_f32_16x16x32_bf16 v[98:101], v[174:177], v[200:203], v[98:101]
	v_mfma_f32_16x16x32_bf16 v[86:89], v[166:169], v[208:211], v[86:89]
	v_mfma_f32_16x16x32_bf16 v[82:85], v[174:177], v[208:211], v[82:85]
	v_mfma_f32_16x16x32_bf16 v[70:73], v[166:169], v[216:219], v[70:73]
	v_mfma_f32_16x16x32_bf16 v[66:69], v[174:177], v[216:219], v[66:69]
	s_barrier
	s_add_i32 s44, s44, s12
	v_lshl_add_u64 v[220:221], s[34:35], 0, v[186:187]
	s_mov_b32 m0, s44
	ds_read_b128 v[178:181], v144 offset:20480
	ds_read_b128 v[182:185], v144 offset:21504
	ds_read_b128 v[196:199], v144 offset:22528
	ds_read_b128 v[200:203], v144 offset:23552
	ds_read_b128 v[204:207], v144 offset:24576
	ds_read_b128 v[208:211], v144 offset:25600
	ds_read_b128 v[212:215], v144 offset:26624
	ds_read_b128 v[216:219], v144 offset:27648
	global_load_lds_dwordx4 v186, s[34:35]
	v_lshl_add_u64 v[222:223], v[220:221], 0, s[82:83]
	s_add_i32 m0, s44, 0x2000
	s_add_i32 s34, s45, s12
	global_load_lds_dwordx4 v[222:223], off
	v_lshl_add_u64 v[222:223], v[220:221], 0, s[64:65]
	s_mov_b32 m0, s34
	v_lshl_add_u64 v[192:193], s[14:15], 0, v[192:193]
	global_load_lds_dwordx4 v[222:223], off
	v_lshl_add_u64 v[222:223], v[220:221], 0, s[86:87]
	s_add_i32 m0, s34, 0x2000
	s_nop 0
	global_load_lds_dwordx4 v[222:223], off
	s_mov_b32 m0, s29
	v_lshl_add_u64 v[222:223], v[192:193], 0, s[82:83]
	global_load_lds_dwordx4 v[192:193], off
	s_mov_b32 m0, s47
	s_nop 0
	global_load_lds_dwordx4 v[222:223], off
	s_waitcnt vmcnt(8)
	s_waitcnt lgkmcnt(0)
	s_barrier
	s_waitcnt lgkmcnt(0)
	v_mfma_f32_16x16x32_bf16 v[62:65], v[146:149], v[178:181], 0
	v_mfma_f32_16x16x32_bf16 v[58:61], v[154:157], v[178:181], 0
	v_mfma_f32_16x16x32_bf16 v[46:49], v[146:149], v[196:199], 0
	v_mfma_f32_16x16x32_bf16 v[42:45], v[154:157], v[196:199], 0
	v_mfma_f32_16x16x32_bf16 v[30:33], v[146:149], v[204:207], 0
	v_mfma_f32_16x16x32_bf16 v[26:29], v[154:157], v[204:207], 0
	v_mfma_f32_16x16x32_bf16 v[14:17], v[146:149], v[212:215], 0
	v_mfma_f32_16x16x32_bf16 v[10:13], v[154:157], v[212:215], 0
	v_mfma_f32_16x16x32_bf16 v[62:65], v[150:153], v[182:185], v[62:65]
	v_mfma_f32_16x16x32_bf16 v[58:61], v[158:161], v[182:185], v[58:61]
	v_mfma_f32_16x16x32_bf16 v[46:49], v[150:153], v[200:203], v[46:49]
	v_mfma_f32_16x16x32_bf16 v[42:45], v[158:161], v[200:203], v[42:45]
	v_mfma_f32_16x16x32_bf16 v[30:33], v[150:153], v[208:211], v[30:33]
	v_mfma_f32_16x16x32_bf16 v[26:29], v[158:161], v[208:211], v[26:29]
	v_mfma_f32_16x16x32_bf16 v[14:17], v[150:153], v[216:219], v[14:17]
	v_mfma_f32_16x16x32_bf16 v[10:13], v[158:161], v[216:219], v[10:13]
	v_mfma_f32_16x16x32_bf16 v[54:57], v[162:165], v[178:181], 0
	v_mfma_f32_16x16x32_bf16 v[50:53], v[170:173], v[178:181], 0
	v_mfma_f32_16x16x32_bf16 v[38:41], v[162:165], v[196:199], 0
	v_mfma_f32_16x16x32_bf16 v[34:37], v[170:173], v[196:199], 0
	v_mfma_f32_16x16x32_bf16 v[22:25], v[162:165], v[204:207], 0
	v_mfma_f32_16x16x32_bf16 v[18:21], v[170:173], v[204:207], 0
	v_mfma_f32_16x16x32_bf16 v[6:9], v[162:165], v[212:215], 0
	v_mfma_f32_16x16x32_bf16 v[2:5], v[170:173], v[212:215], 0
	v_mfma_f32_16x16x32_bf16 v[54:57], v[166:169], v[182:185], v[54:57]
	v_mfma_f32_16x16x32_bf16 v[50:53], v[174:177], v[182:185], v[50:53]
	v_mfma_f32_16x16x32_bf16 v[38:41], v[166:169], v[200:203], v[38:41]
	v_mfma_f32_16x16x32_bf16 v[34:37], v[174:177], v[200:203], v[34:37]
	v_mfma_f32_16x16x32_bf16 v[22:25], v[166:169], v[208:211], v[22:25]
	v_mfma_f32_16x16x32_bf16 v[18:21], v[174:177], v[208:211], v[18:21]
	v_mfma_f32_16x16x32_bf16 v[6:9], v[166:169], v[216:219], v[6:9]
	v_mfma_f32_16x16x32_bf16 v[2:5], v[174:177], v[216:219], v[2:5]
	s_barrier
	s_add_i32 s14, 0, 0x19000
	v_add_u32_e32 v145, s14, v1
	s_add_i32 s15, 0, 0x1d000
	ds_read_b128 v[146:149], v145
	ds_read_b128 v[150:153], v145 offset:1024
	ds_read_b128 v[154:157], v145 offset:2048
	ds_read_b128 v[158:161], v145 offset:3072
	v_add_u32_e32 v145, s15, v1
	ds_read_b128 v[162:165], v145
	ds_read_b128 v[166:169], v145 offset:1024
	ds_read_b128 v[170:173], v145 offset:2048
	ds_read_b128 v[174:177], v145 offset:3072
	s_mov_b32 m0, s60
	v_lshl_add_u64 v[222:223], v[192:193], 0, s[64:65]
	ds_read_b128 v[178:181], v144 offset:36864
	ds_read_b128 v[182:185], v144 offset:37888
	ds_read_b128 v[196:199], v144 offset:38912
	ds_read_b128 v[200:203], v144 offset:39936
	ds_read_b128 v[204:207], v144 offset:40960
	ds_read_b128 v[208:211], v144 offset:41984
	ds_read_b128 v[212:215], v144 offset:43008
	ds_read_b128 v[216:219], v144 offset:44032
	global_load_lds_dwordx4 v[222:223], off
	v_lshl_add_u64 v[222:223], v[192:193], 0, s[86:87]
	s_mov_b32 m0, s61
	s_nop 0
	global_load_lds_dwordx4 v[222:223], off
	s_waitcnt vmcnt(8)
	s_waitcnt lgkmcnt(0)
	s_barrier
	s_waitcnt lgkmcnt(0)
	v_mfma_f32_16x16x32_bf16 v[126:129], v[146:149], v[178:181], v[126:129]
	v_mfma_f32_16x16x32_bf16 v[122:125], v[154:157], v[178:181], v[122:125]
	v_mfma_f32_16x16x32_bf16 v[110:113], v[146:149], v[196:199], v[110:113]
	v_mfma_f32_16x16x32_bf16 v[106:109], v[154:157], v[196:199], v[106:109]
	v_mfma_f32_16x16x32_bf16 v[94:97], v[146:149], v[204:207], v[94:97]
	v_mfma_f32_16x16x32_bf16 v[90:93], v[154:157], v[204:207], v[90:93]
	v_mfma_f32_16x16x32_bf16 v[78:81], v[146:149], v[212:215], v[78:81]
	v_mfma_f32_16x16x32_bf16 v[74:77], v[154:157], v[212:215], v[74:77]
	v_mfma_f32_16x16x32_bf16 v[126:129], v[150:153], v[182:185], v[126:129]
	v_mfma_f32_16x16x32_bf16 v[122:125], v[158:161], v[182:185], v[122:125]
	v_mfma_f32_16x16x32_bf16 v[110:113], v[150:153], v[200:203], v[110:113]
	v_mfma_f32_16x16x32_bf16 v[106:109], v[158:161], v[200:203], v[106:109]
	v_mfma_f32_16x16x32_bf16 v[94:97], v[150:153], v[208:211], v[94:97]
	v_mfma_f32_16x16x32_bf16 v[90:93], v[158:161], v[208:211], v[90:93]
	v_mfma_f32_16x16x32_bf16 v[78:81], v[150:153], v[216:219], v[78:81]
	v_mfma_f32_16x16x32_bf16 v[74:77], v[158:161], v[216:219], v[74:77]
	v_mfma_f32_16x16x32_bf16 v[118:121], v[162:165], v[178:181], v[118:121]
	v_mfma_f32_16x16x32_bf16 v[114:117], v[170:173], v[178:181], v[114:117]
	v_mfma_f32_16x16x32_bf16 v[102:105], v[162:165], v[196:199], v[102:105]
	v_mfma_f32_16x16x32_bf16 v[98:101], v[170:173], v[196:199], v[98:101]
	v_mfma_f32_16x16x32_bf16 v[86:89], v[162:165], v[204:207], v[86:89]
	v_mfma_f32_16x16x32_bf16 v[82:85], v[170:173], v[204:207], v[82:85]
	v_mfma_f32_16x16x32_bf16 v[70:73], v[162:165], v[212:215], v[70:73]
	v_mfma_f32_16x16x32_bf16 v[66:69], v[170:173], v[212:215], v[66:69]
	v_mfma_f32_16x16x32_bf16 v[118:121], v[166:169], v[182:185], v[118:121]
	v_mfma_f32_16x16x32_bf16 v[114:117], v[174:177], v[182:185], v[114:117]
	v_mfma_f32_16x16x32_bf16 v[102:105], v[166:169], v[200:203], v[102:105]
	v_mfma_f32_16x16x32_bf16 v[98:101], v[174:177], v[200:203], v[98:101]
	v_mfma_f32_16x16x32_bf16 v[86:89], v[166:169], v[208:211], v[86:89]
	v_mfma_f32_16x16x32_bf16 v[82:85], v[174:177], v[208:211], v[82:85]
	v_mfma_f32_16x16x32_bf16 v[70:73], v[166:169], v[216:219], v[70:73]
	v_mfma_f32_16x16x32_bf16 v[66:69], v[174:177], v[216:219], v[66:69]
	s_barrier
	s_add_i32 s14, s14, s12
	v_lshl_add_u64 v[222:223], v[220:221], 0, s[92:93]
	s_mov_b32 m0, s14
	ds_read_b128 v[178:181], v144 offset:53248
	ds_read_b128 v[182:185], v144 offset:54272
	ds_read_b128 v[196:199], v144 offset:55296
	ds_read_b128 v[200:203], v144 offset:56320
	ds_read_b128 v[204:207], v144 offset:57344
	ds_read_b128 v[208:211], v144 offset:58368
	ds_read_b128 v[212:215], v144 offset:59392
	ds_read_b128 v[216:219], v144 offset:60416
	global_load_lds_dwordx4 v[222:223], off
	v_lshl_add_u64 v[222:223], v[220:221], 0, s[4:5]
	s_add_i32 m0, s14, 0x2000
	s_add_i32 s14, s15, s12
	global_load_lds_dwordx4 v[222:223], off
	v_lshl_add_u64 v[222:223], v[220:221], 0, s[6:7]
	s_mov_b32 m0, s14
	v_lshl_add_u64 v[220:221], v[220:221], 0, s[8:9]
	global_load_lds_dwordx4 v[222:223], off
	s_add_i32 m0, s14, 0x2000
	s_nop 0
	global_load_lds_dwordx4 v[220:221], off
	v_lshl_add_u64 v[220:221], v[192:193], 0, s[92:93]
	s_mov_b32 m0, s76
	v_lshl_add_u64 v[192:193], v[192:193], 0, s[4:5]
	global_load_lds_dwordx4 v[220:221], off
	s_mov_b32 m0, s77
	s_nop 0
	global_load_lds_dwordx4 v[192:193], off
	s_waitcnt vmcnt(8)
	s_waitcnt lgkmcnt(0)
	s_barrier
	s_waitcnt lgkmcnt(0)
	v_mfma_f32_16x16x32_bf16 v[62:65], v[146:149], v[178:181], v[62:65]
	v_mfma_f32_16x16x32_bf16 v[58:61], v[154:157], v[178:181], v[58:61]
	s_add_i32 s25, s25, 2
	v_mfma_f32_16x16x32_bf16 v[46:49], v[146:149], v[196:199], v[46:49]
	s_add_u32 s42, s42, 0x100
	v_mfma_f32_16x16x32_bf16 v[42:45], v[154:157], v[196:199], v[42:45]
	s_addc_u32 s43, s43, 0
	v_mfma_f32_16x16x32_bf16 v[30:33], v[146:149], v[204:207], v[30:33]
	s_add_u32 s14, s40, s42
	v_mfma_f32_16x16x32_bf16 v[26:29], v[154:157], v[204:207], v[26:29]
	s_addc_u32 s15, s41, s43
	v_mfma_f32_16x16x32_bf16 v[14:17], v[146:149], v[212:215], v[14:17]
	s_add_u32 s34, s14, 0x100
	v_mfma_f32_16x16x32_bf16 v[10:13], v[154:157], v[212:215], v[10:13]
	s_addc_u32 s35, s15, 0
	v_mfma_f32_16x16x32_bf16 v[62:65], v[150:153], v[182:185], v[62:65]
	s_add_u32 s44, s1, s42
	v_mfma_f32_16x16x32_bf16 v[58:61], v[158:161], v[182:185], v[58:61]
	s_addc_u32 s45, s24, s43
	v_mfma_f32_16x16x32_bf16 v[46:49], v[150:153], v[200:203], v[46:49]
	s_cmpk_eq_i32 s42, 0x700
	v_mfma_f32_16x16x32_bf16 v[42:45], v[158:161], v[200:203], v[42:45]
	s_cselect_b64 vcc, -1, 0
	v_mfma_f32_16x16x32_bf16 v[30:33], v[150:153], v[208:211], v[30:33]
	s_and_b64 s[14:15], vcc, exec
	v_mfma_f32_16x16x32_bf16 v[26:29], v[158:161], v[208:211], v[26:29]
	s_cselect_b32 s15, s55, s35
	v_mfma_f32_16x16x32_bf16 v[14:17], v[150:153], v[216:219], v[14:17]
	s_cselect_b32 s14, s54, s34
	v_mfma_f32_16x16x32_bf16 v[10:13], v[158:161], v[216:219], v[10:13]
	s_cselect_b32 s35, s69, s45
	v_mfma_f32_16x16x32_bf16 v[54:57], v[162:165], v[178:181], v[54:57]
	s_cselect_b32 s34, s68, s44
	v_mfma_f32_16x16x32_bf16 v[50:53], v[170:173], v[178:181], v[50:53]
	s_add_i32 s44, 0, 0x11000
	v_mfma_f32_16x16x32_bf16 v[38:41], v[162:165], v[196:199], v[38:41]
	s_add_i32 s45, 0, 0x15000
	v_mfma_f32_16x16x32_bf16 v[34:37], v[170:173], v[196:199], v[34:37]
	v_mfma_f32_16x16x32_bf16 v[22:25], v[162:165], v[204:207], v[22:25]
	v_mfma_f32_16x16x32_bf16 v[18:21], v[170:173], v[204:207], v[18:21]
	v_mfma_f32_16x16x32_bf16 v[6:9], v[162:165], v[212:215], v[6:9]
	v_mfma_f32_16x16x32_bf16 v[2:5], v[170:173], v[212:215], v[2:5]
	v_mfma_f32_16x16x32_bf16 v[54:57], v[166:169], v[182:185], v[54:57]
	v_mfma_f32_16x16x32_bf16 v[50:53], v[174:177], v[182:185], v[50:53]
	v_mfma_f32_16x16x32_bf16 v[38:41], v[166:169], v[200:203], v[38:41]
	v_mfma_f32_16x16x32_bf16 v[34:37], v[174:177], v[200:203], v[34:37]
	v_mfma_f32_16x16x32_bf16 v[22:25], v[166:169], v[208:211], v[22:25]
	v_mfma_f32_16x16x32_bf16 v[18:21], v[174:177], v[208:211], v[18:21]
	v_mfma_f32_16x16x32_bf16 v[6:9], v[166:169], v[216:219], v[6:9]
	v_mfma_f32_16x16x32_bf16 v[2:5], v[174:177], v[216:219], v[2:5]
	s_barrier
.LBB0_391:
	v_add_u32_e32 v145, s44, v1
	ds_read_b128 v[146:149], v145
	ds_read_b128 v[150:153], v145 offset:1024
	ds_read_b128 v[154:157], v145 offset:2048
	ds_read_b128 v[158:161], v145 offset:3072
	v_add_u32_e32 v145, s45, v1
	ds_read_b128 v[162:165], v145
	ds_read_b128 v[166:169], v145 offset:1024
	ds_read_b128 v[170:173], v145 offset:2048
	ds_read_b128 v[174:177], v145 offset:3072
	v_cndmask_b32_e32 v193, v131, v141, vcc
	v_cndmask_b32_e32 v192, v130, v140, vcc
	v_lshl_add_u64 v[220:221], v[142:143], 0, s[42:43]
	v_lshl_add_u64 v[222:223], v[220:221], 0, s[6:7]
	s_add_i32 m0, s28, 0xd000
	ds_read_b128 v[178:181], v144 offset:4096
	ds_read_b128 v[182:185], v144 offset:5120
	ds_read_b128 v[196:199], v144 offset:6144
	ds_read_b128 v[200:203], v144 offset:7168
	ds_read_b128 v[204:207], v144 offset:8192
	ds_read_b128 v[208:211], v144 offset:9216
	ds_read_b128 v[212:215], v144 offset:10240
	ds_read_b128 v[216:219], v144 offset:11264
	global_load_lds_dwordx4 v[222:223], off
	v_lshl_add_u64 v[220:221], v[220:221], 0, s[8:9]
	s_add_i32 m0, s28, 0xf000
	s_nop 0
	global_load_lds_dwordx4 v[220:221], off
	s_waitcnt vmcnt(8)
	s_waitcnt lgkmcnt(0)
	s_barrier
	s_waitcnt lgkmcnt(0)
	v_mfma_f32_16x16x32_bf16 v[126:129], v[146:149], v[178:181], v[126:129]
	v_mfma_f32_16x16x32_bf16 v[122:125], v[154:157], v[178:181], v[122:125]
	v_mfma_f32_16x16x32_bf16 v[110:113], v[146:149], v[196:199], v[110:113]
	v_mfma_f32_16x16x32_bf16 v[106:109], v[154:157], v[196:199], v[106:109]
	v_mfma_f32_16x16x32_bf16 v[94:97], v[146:149], v[204:207], v[94:97]
	v_mfma_f32_16x16x32_bf16 v[90:93], v[154:157], v[204:207], v[90:93]
	v_mfma_f32_16x16x32_bf16 v[78:81], v[146:149], v[212:215], v[78:81]
	v_mfma_f32_16x16x32_bf16 v[74:77], v[154:157], v[212:215], v[74:77]
	v_mfma_f32_16x16x32_bf16 v[126:129], v[150:153], v[182:185], v[126:129]
	v_mfma_f32_16x16x32_bf16 v[122:125], v[158:161], v[182:185], v[122:125]
	v_mfma_f32_16x16x32_bf16 v[110:113], v[150:153], v[200:203], v[110:113]
	v_mfma_f32_16x16x32_bf16 v[106:109], v[158:161], v[200:203], v[106:109]
	v_mfma_f32_16x16x32_bf16 v[94:97], v[150:153], v[208:211], v[94:97]
	v_mfma_f32_16x16x32_bf16 v[90:93], v[158:161], v[208:211], v[90:93]
	v_mfma_f32_16x16x32_bf16 v[78:81], v[150:153], v[216:219], v[78:81]
	v_mfma_f32_16x16x32_bf16 v[74:77], v[158:161], v[216:219], v[74:77]
	v_mfma_f32_16x16x32_bf16 v[118:121], v[162:165], v[178:181], v[118:121]
	v_mfma_f32_16x16x32_bf16 v[114:117], v[170:173], v[178:181], v[114:117]
	v_mfma_f32_16x16x32_bf16 v[102:105], v[162:165], v[196:199], v[102:105]
	v_mfma_f32_16x16x32_bf16 v[98:101], v[170:173], v[196:199], v[98:101]
	v_mfma_f32_16x16x32_bf16 v[86:89], v[162:165], v[204:207], v[86:89]
	v_mfma_f32_16x16x32_bf16 v[82:85], v[170:173], v[204:207], v[82:85]
	v_mfma_f32_16x16x32_bf16 v[70:73], v[162:165], v[212:215], v[70:73]
	v_mfma_f32_16x16x32_bf16 v[66:69], v[170:173], v[212:215], v[66:69]
	v_mfma_f32_16x16x32_bf16 v[118:121], v[166:169], v[182:185], v[118:121]
	v_mfma_f32_16x16x32_bf16 v[114:117], v[174:177], v[182:185], v[114:117]
	v_mfma_f32_16x16x32_bf16 v[102:105], v[166:169], v[200:203], v[102:105]
	v_mfma_f32_16x16x32_bf16 v[98:101], v[174:177], v[200:203], v[98:101]
	v_mfma_f32_16x16x32_bf16 v[86:89], v[166:169], v[208:211], v[86:89]
	v_mfma_f32_16x16x32_bf16 v[82:85], v[174:177], v[208:211], v[82:85]
	v_mfma_f32_16x16x32_bf16 v[70:73], v[166:169], v[216:219], v[70:73]
	v_mfma_f32_16x16x32_bf16 v[66:69], v[174:177], v[216:219], v[66:69]
	s_barrier
	s_add_i32 s44, s44, s12
	v_lshl_add_u64 v[220:221], s[34:35], 0, v[186:187]
	s_mov_b32 m0, s44
	ds_read_b128 v[178:181], v144 offset:20480
	ds_read_b128 v[182:185], v144 offset:21504
	ds_read_b128 v[196:199], v144 offset:22528
	ds_read_b128 v[200:203], v144 offset:23552
	ds_read_b128 v[204:207], v144 offset:24576
	ds_read_b128 v[208:211], v144 offset:25600
	ds_read_b128 v[212:215], v144 offset:26624
	ds_read_b128 v[216:219], v144 offset:27648
	global_load_lds_dwordx4 v186, s[34:35]
	v_lshl_add_u64 v[222:223], v[220:221], 0, s[82:83]
	s_add_i32 m0, s44, 0x2000
	s_add_i32 s34, s45, s12
	global_load_lds_dwordx4 v[222:223], off
	v_lshl_add_u64 v[222:223], v[220:221], 0, s[64:65]
	s_mov_b32 m0, s34
	v_lshl_add_u64 v[192:193], s[14:15], 0, v[192:193]
	global_load_lds_dwordx4 v[222:223], off
	v_lshl_add_u64 v[222:223], v[220:221], 0, s[86:87]
	s_add_i32 m0, s34, 0x2000
	s_nop 0
	global_load_lds_dwordx4 v[222:223], off
	s_mov_b32 m0, s29
	v_lshl_add_u64 v[222:223], v[192:193], 0, s[82:83]
	global_load_lds_dwordx4 v[192:193], off
	s_mov_b32 m0, s47
	s_nop 0
	global_load_lds_dwordx4 v[222:223], off
	s_waitcnt vmcnt(8)
	s_waitcnt lgkmcnt(0)
	s_barrier
	s_waitcnt lgkmcnt(0)
	v_mfma_f32_16x16x32_bf16 v[62:65], v[146:149], v[178:181], v[62:65]
	v_mfma_f32_16x16x32_bf16 v[58:61], v[154:157], v[178:181], v[58:61]
	v_mfma_f32_16x16x32_bf16 v[46:49], v[146:149], v[196:199], v[46:49]
	v_mfma_f32_16x16x32_bf16 v[42:45], v[154:157], v[196:199], v[42:45]
	v_mfma_f32_16x16x32_bf16 v[30:33], v[146:149], v[204:207], v[30:33]
	v_mfma_f32_16x16x32_bf16 v[26:29], v[154:157], v[204:207], v[26:29]
	v_mfma_f32_16x16x32_bf16 v[14:17], v[146:149], v[212:215], v[14:17]
	v_mfma_f32_16x16x32_bf16 v[10:13], v[154:157], v[212:215], v[10:13]
	v_mfma_f32_16x16x32_bf16 v[62:65], v[150:153], v[182:185], v[62:65]
	v_mfma_f32_16x16x32_bf16 v[58:61], v[158:161], v[182:185], v[58:61]
	v_mfma_f32_16x16x32_bf16 v[46:49], v[150:153], v[200:203], v[46:49]
	v_mfma_f32_16x16x32_bf16 v[42:45], v[158:161], v[200:203], v[42:45]
	v_mfma_f32_16x16x32_bf16 v[30:33], v[150:153], v[208:211], v[30:33]
	v_mfma_f32_16x16x32_bf16 v[26:29], v[158:161], v[208:211], v[26:29]
	v_mfma_f32_16x16x32_bf16 v[14:17], v[150:153], v[216:219], v[14:17]
	v_mfma_f32_16x16x32_bf16 v[10:13], v[158:161], v[216:219], v[10:13]
	v_mfma_f32_16x16x32_bf16 v[54:57], v[162:165], v[178:181], v[54:57]
	v_mfma_f32_16x16x32_bf16 v[50:53], v[170:173], v[178:181], v[50:53]
	v_mfma_f32_16x16x32_bf16 v[38:41], v[162:165], v[196:199], v[38:41]
	v_mfma_f32_16x16x32_bf16 v[34:37], v[170:173], v[196:199], v[34:37]
	v_mfma_f32_16x16x32_bf16 v[22:25], v[162:165], v[204:207], v[22:25]
	v_mfma_f32_16x16x32_bf16 v[18:21], v[170:173], v[204:207], v[18:21]
	v_mfma_f32_16x16x32_bf16 v[6:9], v[162:165], v[212:215], v[6:9]
	v_mfma_f32_16x16x32_bf16 v[2:5], v[170:173], v[212:215], v[2:5]
	v_mfma_f32_16x16x32_bf16 v[54:57], v[166:169], v[182:185], v[54:57]
	v_mfma_f32_16x16x32_bf16 v[50:53], v[174:177], v[182:185], v[50:53]
	v_mfma_f32_16x16x32_bf16 v[38:41], v[166:169], v[200:203], v[38:41]
	v_mfma_f32_16x16x32_bf16 v[34:37], v[174:177], v[200:203], v[34:37]
	v_mfma_f32_16x16x32_bf16 v[22:25], v[166:169], v[208:211], v[22:25]
	v_mfma_f32_16x16x32_bf16 v[18:21], v[174:177], v[208:211], v[18:21]
	v_mfma_f32_16x16x32_bf16 v[6:9], v[166:169], v[216:219], v[6:9]
	v_mfma_f32_16x16x32_bf16 v[2:5], v[174:177], v[216:219], v[2:5]
	s_barrier
	s_add_i32 s14, 0, 0x19000
	v_add_u32_e32 v145, s14, v1
	s_add_i32 s15, 0, 0x1d000
	ds_read_b128 v[146:149], v145
	ds_read_b128 v[150:153], v145 offset:1024
	ds_read_b128 v[154:157], v145 offset:2048
	ds_read_b128 v[158:161], v145 offset:3072
	v_add_u32_e32 v145, s15, v1
	ds_read_b128 v[162:165], v145
	ds_read_b128 v[166:169], v145 offset:1024
	ds_read_b128 v[170:173], v145 offset:2048
	ds_read_b128 v[174:177], v145 offset:3072
	s_mov_b32 m0, s60
	v_lshl_add_u64 v[222:223], v[192:193], 0, s[64:65]
	ds_read_b128 v[178:181], v144 offset:36864
	ds_read_b128 v[182:185], v144 offset:37888
	ds_read_b128 v[196:199], v144 offset:38912
	ds_read_b128 v[200:203], v144 offset:39936
	ds_read_b128 v[204:207], v144 offset:40960
	ds_read_b128 v[208:211], v144 offset:41984
	ds_read_b128 v[212:215], v144 offset:43008
	ds_read_b128 v[216:219], v144 offset:44032
	global_load_lds_dwordx4 v[222:223], off
	v_lshl_add_u64 v[222:223], v[192:193], 0, s[86:87]
	s_mov_b32 m0, s61
	s_nop 0
	global_load_lds_dwordx4 v[222:223], off
	s_waitcnt vmcnt(8)
	s_waitcnt lgkmcnt(0)
	s_barrier
	s_waitcnt lgkmcnt(0)
	v_mfma_f32_16x16x32_bf16 v[126:129], v[146:149], v[178:181], v[126:129]
	v_mfma_f32_16x16x32_bf16 v[122:125], v[154:157], v[178:181], v[122:125]
	v_mfma_f32_16x16x32_bf16 v[110:113], v[146:149], v[196:199], v[110:113]
	v_mfma_f32_16x16x32_bf16 v[106:109], v[154:157], v[196:199], v[106:109]
	v_mfma_f32_16x16x32_bf16 v[94:97], v[146:149], v[204:207], v[94:97]
	v_mfma_f32_16x16x32_bf16 v[90:93], v[154:157], v[204:207], v[90:93]
	v_mfma_f32_16x16x32_bf16 v[78:81], v[146:149], v[212:215], v[78:81]
	v_mfma_f32_16x16x32_bf16 v[74:77], v[154:157], v[212:215], v[74:77]
	v_mfma_f32_16x16x32_bf16 v[126:129], v[150:153], v[182:185], v[126:129]
	v_mfma_f32_16x16x32_bf16 v[122:125], v[158:161], v[182:185], v[122:125]
	v_mfma_f32_16x16x32_bf16 v[110:113], v[150:153], v[200:203], v[110:113]
	v_mfma_f32_16x16x32_bf16 v[106:109], v[158:161], v[200:203], v[106:109]
	v_mfma_f32_16x16x32_bf16 v[94:97], v[150:153], v[208:211], v[94:97]
	v_mfma_f32_16x16x32_bf16 v[90:93], v[158:161], v[208:211], v[90:93]
	v_mfma_f32_16x16x32_bf16 v[78:81], v[150:153], v[216:219], v[78:81]
	v_mfma_f32_16x16x32_bf16 v[74:77], v[158:161], v[216:219], v[74:77]
	v_mfma_f32_16x16x32_bf16 v[118:121], v[162:165], v[178:181], v[118:121]
	v_mfma_f32_16x16x32_bf16 v[114:117], v[170:173], v[178:181], v[114:117]
	v_mfma_f32_16x16x32_bf16 v[102:105], v[162:165], v[196:199], v[102:105]
	v_mfma_f32_16x16x32_bf16 v[98:101], v[170:173], v[196:199], v[98:101]
	v_mfma_f32_16x16x32_bf16 v[86:89], v[162:165], v[204:207], v[86:89]
	v_mfma_f32_16x16x32_bf16 v[82:85], v[170:173], v[204:207], v[82:85]
	v_mfma_f32_16x16x32_bf16 v[70:73], v[162:165], v[212:215], v[70:73]
	v_mfma_f32_16x16x32_bf16 v[66:69], v[170:173], v[212:215], v[66:69]
	v_mfma_f32_16x16x32_bf16 v[118:121], v[166:169], v[182:185], v[118:121]
	v_mfma_f32_16x16x32_bf16 v[114:117], v[174:177], v[182:185], v[114:117]
	v_mfma_f32_16x16x32_bf16 v[102:105], v[166:169], v[200:203], v[102:105]
	v_mfma_f32_16x16x32_bf16 v[98:101], v[174:177], v[200:203], v[98:101]
	v_mfma_f32_16x16x32_bf16 v[86:89], v[166:169], v[208:211], v[86:89]
	v_mfma_f32_16x16x32_bf16 v[82:85], v[174:177], v[208:211], v[82:85]
	v_mfma_f32_16x16x32_bf16 v[70:73], v[166:169], v[216:219], v[70:73]
	v_mfma_f32_16x16x32_bf16 v[66:69], v[174:177], v[216:219], v[66:69]
	s_barrier
	s_add_i32 s14, s14, s12
	v_lshl_add_u64 v[222:223], v[220:221], 0, s[92:93]
	s_mov_b32 m0, s14
	ds_read_b128 v[178:181], v144 offset:53248
	ds_read_b128 v[182:185], v144 offset:54272
	ds_read_b128 v[196:199], v144 offset:55296
	ds_read_b128 v[200:203], v144 offset:56320
	ds_read_b128 v[204:207], v144 offset:57344
	ds_read_b128 v[208:211], v144 offset:58368
	ds_read_b128 v[212:215], v144 offset:59392
	ds_read_b128 v[216:219], v144 offset:60416
	global_load_lds_dwordx4 v[222:223], off
	v_lshl_add_u64 v[222:223], v[220:221], 0, s[4:5]
	s_add_i32 m0, s14, 0x2000
	s_add_i32 s14, s15, s12
	global_load_lds_dwordx4 v[222:223], off
	v_lshl_add_u64 v[222:223], v[220:221], 0, s[6:7]
	s_mov_b32 m0, s14
	v_lshl_add_u64 v[220:221], v[220:221], 0, s[8:9]
	global_load_lds_dwordx4 v[222:223], off
	s_add_i32 m0, s14, 0x2000
	s_nop 0
	global_load_lds_dwordx4 v[220:221], off
	v_lshl_add_u64 v[220:221], v[192:193], 0, s[92:93]
	s_mov_b32 m0, s76
	v_lshl_add_u64 v[192:193], v[192:193], 0, s[4:5]
	global_load_lds_dwordx4 v[220:221], off
	s_mov_b32 m0, s77
	s_nop 0
	global_load_lds_dwordx4 v[192:193], off
	s_waitcnt vmcnt(8)
	s_waitcnt lgkmcnt(0)
	s_barrier
	s_waitcnt lgkmcnt(0)
	v_mfma_f32_16x16x32_bf16 v[62:65], v[146:149], v[178:181], v[62:65]
	v_mfma_f32_16x16x32_bf16 v[58:61], v[154:157], v[178:181], v[58:61]
	s_add_i32 s25, s25, 2
	v_mfma_f32_16x16x32_bf16 v[46:49], v[146:149], v[196:199], v[46:49]
	s_add_u32 s42, s42, 0x100
	v_mfma_f32_16x16x32_bf16 v[42:45], v[154:157], v[196:199], v[42:45]
	s_addc_u32 s43, s43, 0
	v_mfma_f32_16x16x32_bf16 v[30:33], v[146:149], v[204:207], v[30:33]
	s_add_u32 s14, s40, s42
	v_mfma_f32_16x16x32_bf16 v[26:29], v[154:157], v[204:207], v[26:29]
	s_addc_u32 s15, s41, s43
	v_mfma_f32_16x16x32_bf16 v[14:17], v[146:149], v[212:215], v[14:17]
	s_add_u32 s34, s14, 0x100
	v_mfma_f32_16x16x32_bf16 v[10:13], v[154:157], v[212:215], v[10:13]
	s_addc_u32 s35, s15, 0
	v_mfma_f32_16x16x32_bf16 v[62:65], v[150:153], v[182:185], v[62:65]
	s_add_u32 s44, s1, s42
	v_mfma_f32_16x16x32_bf16 v[58:61], v[158:161], v[182:185], v[58:61]
	s_addc_u32 s45, s24, s43
	v_mfma_f32_16x16x32_bf16 v[46:49], v[150:153], v[200:203], v[46:49]
	s_cmpk_eq_i32 s42, 0x700
	v_mfma_f32_16x16x32_bf16 v[42:45], v[158:161], v[200:203], v[42:45]
	s_cselect_b64 vcc, -1, 0
	v_mfma_f32_16x16x32_bf16 v[30:33], v[150:153], v[208:211], v[30:33]
	s_and_b64 s[14:15], vcc, exec
	v_mfma_f32_16x16x32_bf16 v[26:29], v[158:161], v[208:211], v[26:29]
	s_cselect_b32 s15, s55, s35
	v_mfma_f32_16x16x32_bf16 v[14:17], v[150:153], v[216:219], v[14:17]
	s_cselect_b32 s14, s54, s34
	v_mfma_f32_16x16x32_bf16 v[10:13], v[158:161], v[216:219], v[10:13]
	s_cselect_b32 s35, s69, s45
	v_mfma_f32_16x16x32_bf16 v[54:57], v[162:165], v[178:181], v[54:57]
	s_cselect_b32 s34, s68, s44
	v_mfma_f32_16x16x32_bf16 v[50:53], v[170:173], v[178:181], v[50:53]
	s_add_i32 s44, 0, 0x11000
	v_mfma_f32_16x16x32_bf16 v[38:41], v[162:165], v[196:199], v[38:41]
	s_add_i32 s45, 0, 0x15000
	v_mfma_f32_16x16x32_bf16 v[34:37], v[170:173], v[196:199], v[34:37]
	v_mfma_f32_16x16x32_bf16 v[22:25], v[162:165], v[204:207], v[22:25]
	v_mfma_f32_16x16x32_bf16 v[18:21], v[170:173], v[204:207], v[18:21]
	v_mfma_f32_16x16x32_bf16 v[6:9], v[162:165], v[212:215], v[6:9]
	v_mfma_f32_16x16x32_bf16 v[2:5], v[170:173], v[212:215], v[2:5]
	v_mfma_f32_16x16x32_bf16 v[54:57], v[166:169], v[182:185], v[54:57]
	v_mfma_f32_16x16x32_bf16 v[50:53], v[174:177], v[182:185], v[50:53]
	v_mfma_f32_16x16x32_bf16 v[38:41], v[166:169], v[200:203], v[38:41]
	v_mfma_f32_16x16x32_bf16 v[34:37], v[174:177], v[200:203], v[34:37]
	v_mfma_f32_16x16x32_bf16 v[22:25], v[166:169], v[208:211], v[22:25]
	v_mfma_f32_16x16x32_bf16 v[18:21], v[174:177], v[208:211], v[18:21]
	v_mfma_f32_16x16x32_bf16 v[6:9], v[166:169], v[216:219], v[6:9]
	v_mfma_f32_16x16x32_bf16 v[2:5], v[174:177], v[216:219], v[2:5]
	s_barrier
	s_cmp_gt_u32 s25, 13
	s_cbranch_scc0 .LBB0_391
	s_setprio 0
	s_and_b64 vcc, exec, s[50:51]
	s_cbranch_vccz .LBB0_394
	s_barrier

.LBB0_1110:
	s_andn2_b64 vcc, exec, s[0:1]
	s_cbranch_vccnz .Lprio_out
	s_setprio 1
.Lprio_out:
	s_add_u32 s24, s54, 0x100
	v_lshl_add_u64 v[140:141], s[52:53], 0, v[138:139]
	s_addc_u32 s25, s55, 0
	s_mov_b32 s43, -2
	s_mov_b64 s[54:55], 0
	s_add_u32 s14, s52, s54
	s_addc_u32 s15, s53, s55
	s_add_u32 s45, s14, 0x100
	s_addc_u32 s73, s15, 0
	s_add_u32 s74, s24, s54
	s_addc_u32 s75, s25, s55
	s_cmpk_eq_i32 s54, 0x700
	s_cselect_b64 vcc, -1, 0
	s_and_b64 s[14:15], vcc, exec
	s_cselect_b32 s15, s47, s73
	s_cselect_b32 s14, s46, s45
	s_cselect_b32 s75, s49, s75
	s_cselect_b32 s74, s48, s74
	s_add_i32 s45, 0, 0x11000
	v_add_u32_e32 v131, s45, v1
	s_add_i32 s73, 0, 0x15000
	ds_read_b128 v[144:147], v131
	ds_read_b128 v[148:151], v131 offset:1024
	ds_read_b128 v[152:155], v131 offset:2048
	ds_read_b128 v[156:159], v131 offset:3072
	v_add_u32_e32 v131, s73, v1
	ds_read_b128 v[160:163], v131
	ds_read_b128 v[164:167], v131 offset:1024
	ds_read_b128 v[168:171], v131 offset:2048
	ds_read_b128 v[172:175], v131 offset:3072
	v_cndmask_b32_e32 v185, v139, v137, vcc
	v_cndmask_b32_e32 v184, v138, v136, vcc
	v_lshl_add_u64 v[192:193], v[140:141], 0, s[54:55]
	v_lshl_add_u64 v[220:221], v[192:193], 0, s[6:7]
	s_add_i32 m0, s29, 0xd000
	ds_read_b128 v[176:179], v142 offset:4096
	ds_read_b128 v[180:183], v142 offset:5120
	ds_read_b128 v[196:199], v142 offset:6144
	ds_read_b128 v[200:203], v142 offset:7168
	ds_read_b128 v[204:207], v142 offset:8192
	ds_read_b128 v[208:211], v142 offset:9216
	ds_read_b128 v[212:215], v142 offset:10240
	ds_read_b128 v[216:219], v142 offset:11264
	global_load_lds_dwordx4 v[220:221], off
	v_lshl_add_u64 v[192:193], v[192:193], 0, s[8:9]
	s_add_i32 m0, s29, 0xf000
	s_nop 0
	global_load_lds_dwordx4 v[192:193], off
	s_waitcnt vmcnt(8)
	s_waitcnt lgkmcnt(0)
	s_barrier
	s_waitcnt lgkmcnt(0)
	v_mfma_f32_16x16x32_bf16 v[126:129], v[144:147], v[176:179], 0
	v_mfma_f32_16x16x32_bf16 v[122:125], v[152:155], v[176:179], 0
	v_mfma_f32_16x16x32_bf16 v[110:113], v[144:147], v[196:199], 0
	v_mfma_f32_16x16x32_bf16 v[106:109], v[152:155], v[196:199], 0
	v_mfma_f32_16x16x32_bf16 v[94:97], v[144:147], v[204:207], 0
	v_mfma_f32_16x16x32_bf16 v[90:93], v[152:155], v[204:207], 0
	v_mfma_f32_16x16x32_bf16 v[78:81], v[144:147], v[212:215], 0
	v_mfma_f32_16x16x32_bf16 v[74:77], v[152:155], v[212:215], 0
	v_mfma_f32_16x16x32_bf16 v[126:129], v[148:151], v[180:183], v[126:129]
	v_mfma_f32_16x16x32_bf16 v[122:125], v[156:159], v[180:183], v[122:125]
	v_mfma_f32_16x16x32_bf16 v[110:113], v[148:151], v[200:203], v[110:113]
	v_mfma_f32_16x16x32_bf16 v[106:109], v[156:159], v[200:203], v[106:109]
	v_mfma_f32_16x16x32_bf16 v[94:97], v[148:151], v[208:211], v[94:97]
	v_mfma_f32_16x16x32_bf16 v[90:93], v[156:159], v[208:211], v[90:93]
	v_mfma_f32_16x16x32_bf16 v[78:81], v[148:151], v[216:219], v[78:81]
	v_mfma_f32_16x16x32_bf16 v[74:77], v[156:159], v[216:219], v[74:77]
	v_mfma_f32_16x16x32_bf16 v[118:121], v[160:163], v[176:179], 0
	v_mfma_f32_16x16x32_bf16 v[114:117], v[168:171], v[176:179], 0
	v_mfma_f32_16x16x32_bf16 v[102:105], v[160:163], v[196:199], 0
	v_mfma_f32_16x16x32_bf16 v[98:101], v[168:171], v[196:199], 0
	v_mfma_f32_16x16x32_bf16 v[86:89], v[160:163], v[204:207], 0
	v_mfma_f32_16x16x32_bf16 v[82:85], v[168:171], v[204:207], 0
	v_mfma_f32_16x16x32_bf16 v[70:73], v[160:163], v[212:215], 0
	v_mfma_f32_16x16x32_bf16 v[66:69], v[168:171], v[212:215], 0
	v_mfma_f32_16x16x32_bf16 v[118:121], v[164:167], v[180:183], v[118:121]
	v_mfma_f32_16x16x32_bf16 v[114:117], v[172:175], v[180:183], v[114:117]
	v_mfma_f32_16x16x32_bf16 v[102:105], v[164:167], v[200:203], v[102:105]
	v_mfma_f32_16x16x32_bf16 v[98:101], v[172:175], v[200:203], v[98:101]
	v_mfma_f32_16x16x32_bf16 v[86:89], v[164:167], v[208:211], v[86:89]
	v_mfma_f32_16x16x32_bf16 v[82:85], v[172:175], v[208:211], v[82:85]
	v_mfma_f32_16x16x32_bf16 v[70:73], v[164:167], v[216:219], v[70:73]
	v_mfma_f32_16x16x32_bf16 v[66:69], v[172:175], v[216:219], v[66:69]
	s_barrier
	s_add_i32 s45, s45, s2
	v_lshl_add_u64 v[192:193], s[74:75], 0, v[186:187]
	s_mov_b32 m0, s45
	ds_read_b128 v[176:179], v142 offset:20480
	ds_read_b128 v[180:183], v142 offset:21504
	ds_read_b128 v[196:199], v142 offset:22528
	ds_read_b128 v[200:203], v142 offset:23552
	ds_read_b128 v[204:207], v142 offset:24576
	ds_read_b128 v[208:211], v142 offset:25600
	ds_read_b128 v[212:215], v142 offset:26624
	ds_read_b128 v[216:219], v142 offset:27648
	global_load_lds_dwordx4 v186, s[74:75]
	v_lshl_add_u64 v[220:221], v[192:193], 0, s[82:83]
	s_add_i32 m0, s45, 0x2000
	s_add_i32 s45, s73, s2
	global_load_lds_dwordx4 v[220:221], off
	v_lshl_add_u64 v[220:221], v[192:193], 0, s[64:65]
	s_mov_b32 m0, s45
	v_lshl_add_u64 v[184:185], s[14:15], 0, v[184:185]
	global_load_lds_dwordx4 v[220:221], off
	v_lshl_add_u64 v[220:221], v[192:193], 0, s[86:87]
	s_add_i32 m0, s45, 0x2000
	s_nop 0
	global_load_lds_dwordx4 v[220:221], off
	s_mov_b32 m0, s33
	v_lshl_add_u64 v[220:221], v[184:185], 0, s[82:83]
	global_load_lds_dwordx4 v[184:185], off
	s_mov_b32 m0, s34
	s_nop 0
	global_load_lds_dwordx4 v[220:221], off
	s_waitcnt vmcnt(8)
	s_waitcnt lgkmcnt(0)
	s_barrier
	s_waitcnt lgkmcnt(0)
	v_mfma_f32_16x16x32_bf16 v[62:65], v[144:147], v[176:179], 0
	v_mfma_f32_16x16x32_bf16 v[58:61], v[152:155], v[176:179], 0
	v_mfma_f32_16x16x32_bf16 v[46:49], v[144:147], v[196:199], 0
	v_mfma_f32_16x16x32_bf16 v[42:45], v[152:155], v[196:199], 0
	v_mfma_f32_16x16x32_bf16 v[30:33], v[144:147], v[204:207], 0
	v_mfma_f32_16x16x32_bf16 v[26:29], v[152:155], v[204:207], 0
	v_mfma_f32_16x16x32_bf16 v[14:17], v[144:147], v[212:215], 0
	v_mfma_f32_16x16x32_bf16 v[10:13], v[152:155], v[212:215], 0
	v_mfma_f32_16x16x32_bf16 v[62:65], v[148:151], v[180:183], v[62:65]
	v_mfma_f32_16x16x32_bf16 v[58:61], v[156:159], v[180:183], v[58:61]
	v_mfma_f32_16x16x32_bf16 v[46:49], v[148:151], v[200:203], v[46:49]
	v_mfma_f32_16x16x32_bf16 v[42:45], v[156:159], v[200:203], v[42:45]
	v_mfma_f32_16x16x32_bf16 v[30:33], v[148:151], v[208:211], v[30:33]
	v_mfma_f32_16x16x32_bf16 v[26:29], v[156:159], v[208:211], v[26:29]
	v_mfma_f32_16x16x32_bf16 v[14:17], v[148:151], v[216:219], v[14:17]
	v_mfma_f32_16x16x32_bf16 v[10:13], v[156:159], v[216:219], v[10:13]
	v_mfma_f32_16x16x32_bf16 v[54:57], v[160:163], v[176:179], 0
	v_mfma_f32_16x16x32_bf16 v[50:53], v[168:171], v[176:179], 0
	v_mfma_f32_16x16x32_bf16 v[38:41], v[160:163], v[196:199], 0
	v_mfma_f32_16x16x32_bf16 v[34:37], v[168:171], v[196:199], 0
	v_mfma_f32_16x16x32_bf16 v[22:25], v[160:163], v[204:207], 0
	v_mfma_f32_16x16x32_bf16 v[18:21], v[168:171], v[204:207], 0
	v_mfma_f32_16x16x32_bf16 v[6:9], v[160:163], v[212:215], 0
	v_mfma_f32_16x16x32_bf16 v[2:5], v[168:171], v[212:215], 0
	v_mfma_f32_16x16x32_bf16 v[54:57], v[164:167], v[180:183], v[54:57]
	v_mfma_f32_16x16x32_bf16 v[50:53], v[172:175], v[180:183], v[50:53]
	v_mfma_f32_16x16x32_bf16 v[38:41], v[164:167], v[200:203], v[38:41]
	v_mfma_f32_16x16x32_bf16 v[34:37], v[172:175], v[200:203], v[34:37]
	v_mfma_f32_16x16x32_bf16 v[22:25], v[164:167], v[208:211], v[22:25]
	v_mfma_f32_16x16x32_bf16 v[18:21], v[172:175], v[208:211], v[18:21]
	v_mfma_f32_16x16x32_bf16 v[6:9], v[164:167], v[216:219], v[6:9]
	v_mfma_f32_16x16x32_bf16 v[2:5], v[172:175], v[216:219], v[2:5]
	s_barrier
	s_add_i32 s14, 0, 0x19000
	v_add_u32_e32 v131, s14, v1
	s_add_i32 s15, 0, 0x1d000
	ds_read_b128 v[144:147], v131
	ds_read_b128 v[148:151], v131 offset:1024
	ds_read_b128 v[152:155], v131 offset:2048
	ds_read_b128 v[156:159], v131 offset:3072
	v_add_u32_e32 v131, s15, v1
	ds_read_b128 v[160:163], v131
	ds_read_b128 v[164:167], v131 offset:1024
	ds_read_b128 v[168:171], v131 offset:2048
	ds_read_b128 v[172:175], v131 offset:3072
	s_mov_b32 m0, s35
	v_lshl_add_u64 v[220:221], v[184:185], 0, s[64:65]
	ds_read_b128 v[176:179], v142 offset:36864
	ds_read_b128 v[180:183], v142 offset:37888
	ds_read_b128 v[196:199], v142 offset:38912
	ds_read_b128 v[200:203], v142 offset:39936
	ds_read_b128 v[204:207], v142 offset:40960
	ds_read_b128 v[208:211], v142 offset:41984
	ds_read_b128 v[212:215], v142 offset:43008
	ds_read_b128 v[216:219], v142 offset:44032
	global_load_lds_dwordx4 v[220:221], off
	v_lshl_add_u64 v[220:221], v[184:185], 0, s[86:87]
	s_mov_b32 m0, s56
	s_nop 0
	global_load_lds_dwordx4 v[220:221], off
	s_waitcnt vmcnt(8)
	s_waitcnt lgkmcnt(0)
	s_barrier
	s_waitcnt lgkmcnt(0)
	v_mfma_f32_16x16x32_bf16 v[126:129], v[144:147], v[176:179], v[126:129]
	v_mfma_f32_16x16x32_bf16 v[122:125], v[152:155], v[176:179], v[122:125]
	v_mfma_f32_16x16x32_bf16 v[110:113], v[144:147], v[196:199], v[110:113]
	v_mfma_f32_16x16x32_bf16 v[106:109], v[152:155], v[196:199], v[106:109]
	v_mfma_f32_16x16x32_bf16 v[94:97], v[144:147], v[204:207], v[94:97]
	v_mfma_f32_16x16x32_bf16 v[90:93], v[152:155], v[204:207], v[90:93]
	v_mfma_f32_16x16x32_bf16 v[78:81], v[144:147], v[212:215], v[78:81]
	v_mfma_f32_16x16x32_bf16 v[74:77], v[152:155], v[212:215], v[74:77]
	v_mfma_f32_16x16x32_bf16 v[126:129], v[148:151], v[180:183], v[126:129]
	v_mfma_f32_16x16x32_bf16 v[122:125], v[156:159], v[180:183], v[122:125]
	v_mfma_f32_16x16x32_bf16 v[110:113], v[148:151], v[200:203], v[110:113]
	v_mfma_f32_16x16x32_bf16 v[106:109], v[156:159], v[200:203], v[106:109]
	v_mfma_f32_16x16x32_bf16 v[94:97], v[148:151], v[208:211], v[94:97]
	v_mfma_f32_16x16x32_bf16 v[90:93], v[156:159], v[208:211], v[90:93]
	v_mfma_f32_16x16x32_bf16 v[78:81], v[148:151], v[216:219], v[78:81]
	v_mfma_f32_16x16x32_bf16 v[74:77], v[156:159], v[216:219], v[74:77]
	v_mfma_f32_16x16x32_bf16 v[118:121], v[160:163], v[176:179], v[118:121]
	v_mfma_f32_16x16x32_bf16 v[114:117], v[168:171], v[176:179], v[114:117]
	v_mfma_f32_16x16x32_bf16 v[102:105], v[160:163], v[196:199], v[102:105]
	v_mfma_f32_16x16x32_bf16 v[98:101], v[168:171], v[196:199], v[98:101]
	v_mfma_f32_16x16x32_bf16 v[86:89], v[160:163], v[204:207], v[86:89]
	v_mfma_f32_16x16x32_bf16 v[82:85], v[168:171], v[204:207], v[82:85]
	v_mfma_f32_16x16x32_bf16 v[70:73], v[160:163], v[212:215], v[70:73]
	v_mfma_f32_16x16x32_bf16 v[66:69], v[168:171], v[212:215], v[66:69]
	v_mfma_f32_16x16x32_bf16 v[118:121], v[164:167], v[180:183], v[118:121]
	v_mfma_f32_16x16x32_bf16 v[114:117], v[172:175], v[180:183], v[114:117]
	v_mfma_f32_16x16x32_bf16 v[102:105], v[164:167], v[200:203], v[102:105]
	v_mfma_f32_16x16x32_bf16 v[98:101], v[172:175], v[200:203], v[98:101]
	v_mfma_f32_16x16x32_bf16 v[86:89], v[164:167], v[208:211], v[86:89]
	v_mfma_f32_16x16x32_bf16 v[82:85], v[172:175], v[208:211], v[82:85]
	v_mfma_f32_16x16x32_bf16 v[70:73], v[164:167], v[216:219], v[70:73]
	v_mfma_f32_16x16x32_bf16 v[66:69], v[172:175], v[216:219], v[66:69]
	s_barrier
	s_add_i32 s14, s14, s2
	v_lshl_add_u64 v[220:221], v[192:193], 0, s[92:93]
	s_mov_b32 m0, s14
	ds_read_b128 v[176:179], v142 offset:53248
	ds_read_b128 v[180:183], v142 offset:54272
	ds_read_b128 v[196:199], v142 offset:55296
	ds_read_b128 v[200:203], v142 offset:56320
	ds_read_b128 v[204:207], v142 offset:57344
	ds_read_b128 v[208:211], v142 offset:58368
	ds_read_b128 v[212:215], v142 offset:59392
	ds_read_b128 v[216:219], v142 offset:60416
	global_load_lds_dwordx4 v[220:221], off
	v_lshl_add_u64 v[220:221], v[192:193], 0, s[4:5]
	s_add_i32 m0, s14, 0x2000
	s_add_i32 s14, s15, s2
	global_load_lds_dwordx4 v[220:221], off
	v_lshl_add_u64 v[220:221], v[192:193], 0, s[6:7]
	s_mov_b32 m0, s14
	v_lshl_add_u64 v[192:193], v[192:193], 0, s[8:9]
	global_load_lds_dwordx4 v[220:221], off
	s_add_i32 m0, s14, 0x2000
	s_nop 0
	global_load_lds_dwordx4 v[192:193], off
	v_lshl_add_u64 v[192:193], v[184:185], 0, s[92:93]
	s_mov_b32 m0, s59
	v_lshl_add_u64 v[184:185], v[184:185], 0, s[4:5]
	global_load_lds_dwordx4 v[192:193], off
	s_mov_b32 m0, s60
	s_nop 0
	global_load_lds_dwordx4 v[184:185], off
	s_waitcnt vmcnt(8)
	s_waitcnt lgkmcnt(0)
	s_barrier
	s_waitcnt lgkmcnt(0)
	v_mfma_f32_16x16x32_bf16 v[62:65], v[144:147], v[176:179], v[62:65]
	v_mfma_f32_16x16x32_bf16 v[58:61], v[152:155], v[176:179], v[58:61]
	s_add_i32 s43, s43, 2
	v_mfma_f32_16x16x32_bf16 v[46:49], v[144:147], v[196:199], v[46:49]
	s_add_u32 s54, s54, 0x100
	v_mfma_f32_16x16x32_bf16 v[42:45], v[152:155], v[196:199], v[42:45]
	s_addc_u32 s55, s55, 0
	v_mfma_f32_16x16x32_bf16 v[30:33], v[144:147], v[204:207], v[30:33]
	s_add_u32 s14, s52, s54
	v_mfma_f32_16x16x32_bf16 v[26:29], v[152:155], v[204:207], v[26:29]
	s_addc_u32 s15, s53, s55
	v_mfma_f32_16x16x32_bf16 v[14:17], v[144:147], v[212:215], v[14:17]
	s_add_u32 s45, s14, 0x100
	v_mfma_f32_16x16x32_bf16 v[10:13], v[152:155], v[212:215], v[10:13]
	s_addc_u32 s73, s15, 0
	v_mfma_f32_16x16x32_bf16 v[62:65], v[148:151], v[180:183], v[62:65]
	s_add_u32 s74, s24, s54
	v_mfma_f32_16x16x32_bf16 v[58:61], v[156:159], v[180:183], v[58:61]
	s_addc_u32 s75, s25, s55
	v_mfma_f32_16x16x32_bf16 v[46:49], v[148:151], v[200:203], v[46:49]
	s_cmpk_eq_i32 s54, 0x700
	v_mfma_f32_16x16x32_bf16 v[42:45], v[156:159], v[200:203], v[42:45]
	s_cselect_b64 vcc, -1, 0
	v_mfma_f32_16x16x32_bf16 v[30:33], v[148:151], v[208:211], v[30:33]
	s_and_b64 s[14:15], vcc, exec
	v_mfma_f32_16x16x32_bf16 v[26:29], v[156:159], v[208:211], v[26:29]
	s_cselect_b32 s15, s47, s73
	v_mfma_f32_16x16x32_bf16 v[14:17], v[148:151], v[216:219], v[14:17]
	s_cselect_b32 s14, s46, s45
	v_mfma_f32_16x16x32_bf16 v[10:13], v[156:159], v[216:219], v[10:13]
	s_cselect_b32 s75, s49, s75
	v_mfma_f32_16x16x32_bf16 v[54:57], v[160:163], v[176:179], v[54:57]
	s_cselect_b32 s74, s48, s74
	v_mfma_f32_16x16x32_bf16 v[50:53], v[168:171], v[176:179], v[50:53]
	s_add_i32 s45, 0, 0x11000
	v_mfma_f32_16x16x32_bf16 v[38:41], v[160:163], v[196:199], v[38:41]
	s_add_i32 s73, 0, 0x15000
	v_mfma_f32_16x16x32_bf16 v[34:37], v[168:171], v[196:199], v[34:37]
	v_mfma_f32_16x16x32_bf16 v[22:25], v[160:163], v[204:207], v[22:25]
	v_mfma_f32_16x16x32_bf16 v[18:21], v[168:171], v[204:207], v[18:21]
	v_mfma_f32_16x16x32_bf16 v[6:9], v[160:163], v[212:215], v[6:9]
	v_mfma_f32_16x16x32_bf16 v[2:5], v[168:171], v[212:215], v[2:5]
	v_mfma_f32_16x16x32_bf16 v[54:57], v[164:167], v[180:183], v[54:57]
	v_mfma_f32_16x16x32_bf16 v[50:53], v[172:175], v[180:183], v[50:53]
	v_mfma_f32_16x16x32_bf16 v[38:41], v[164:167], v[200:203], v[38:41]
	v_mfma_f32_16x16x32_bf16 v[34:37], v[172:175], v[200:203], v[34:37]
	v_mfma_f32_16x16x32_bf16 v[22:25], v[164:167], v[208:211], v[22:25]
	v_mfma_f32_16x16x32_bf16 v[18:21], v[172:175], v[208:211], v[18:21]
	v_mfma_f32_16x16x32_bf16 v[6:9], v[164:167], v[216:219], v[6:9]
	v_mfma_f32_16x16x32_bf16 v[2:5], v[172:175], v[216:219], v[2:5]
	s_barrier
.LBB0_1111:
	v_add_u32_e32 v131, s45, v1
	ds_read_b128 v[144:147], v131
	ds_read_b128 v[148:151], v131 offset:1024
	ds_read_b128 v[152:155], v131 offset:2048
	ds_read_b128 v[156:159], v131 offset:3072
	v_add_u32_e32 v131, s73, v1
	ds_read_b128 v[160:163], v131
	ds_read_b128 v[164:167], v131 offset:1024
	ds_read_b128 v[168:171], v131 offset:2048
	ds_read_b128 v[172:175], v131 offset:3072
	v_cndmask_b32_e32 v185, v139, v137, vcc
	v_cndmask_b32_e32 v184, v138, v136, vcc
	v_lshl_add_u64 v[192:193], v[140:141], 0, s[54:55]
	v_lshl_add_u64 v[220:221], v[192:193], 0, s[6:7]
	s_add_i32 m0, s29, 0xd000
	ds_read_b128 v[176:179], v142 offset:4096
	ds_read_b128 v[180:183], v142 offset:5120
	ds_read_b128 v[196:199], v142 offset:6144
	ds_read_b128 v[200:203], v142 offset:7168
	ds_read_b128 v[204:207], v142 offset:8192
	ds_read_b128 v[208:211], v142 offset:9216
	ds_read_b128 v[212:215], v142 offset:10240
	ds_read_b128 v[216:219], v142 offset:11264
	global_load_lds_dwordx4 v[220:221], off
	v_lshl_add_u64 v[192:193], v[192:193], 0, s[8:9]
	s_add_i32 m0, s29, 0xf000
	s_nop 0
	global_load_lds_dwordx4 v[192:193], off
	s_waitcnt vmcnt(8)
	s_waitcnt lgkmcnt(0)
	s_barrier
	s_waitcnt lgkmcnt(0)
	v_mfma_f32_16x16x32_bf16 v[126:129], v[144:147], v[176:179], v[126:129]
	v_mfma_f32_16x16x32_bf16 v[122:125], v[152:155], v[176:179], v[122:125]
	v_mfma_f32_16x16x32_bf16 v[110:113], v[144:147], v[196:199], v[110:113]
	v_mfma_f32_16x16x32_bf16 v[106:109], v[152:155], v[196:199], v[106:109]
	v_mfma_f32_16x16x32_bf16 v[94:97], v[144:147], v[204:207], v[94:97]
	v_mfma_f32_16x16x32_bf16 v[90:93], v[152:155], v[204:207], v[90:93]
	v_mfma_f32_16x16x32_bf16 v[78:81], v[144:147], v[212:215], v[78:81]
	v_mfma_f32_16x16x32_bf16 v[74:77], v[152:155], v[212:215], v[74:77]
	v_mfma_f32_16x16x32_bf16 v[126:129], v[148:151], v[180:183], v[126:129]
	v_mfma_f32_16x16x32_bf16 v[122:125], v[156:159], v[180:183], v[122:125]
	v_mfma_f32_16x16x32_bf16 v[110:113], v[148:151], v[200:203], v[110:113]
	v_mfma_f32_16x16x32_bf16 v[106:109], v[156:159], v[200:203], v[106:109]
	v_mfma_f32_16x16x32_bf16 v[94:97], v[148:151], v[208:211], v[94:97]
	v_mfma_f32_16x16x32_bf16 v[90:93], v[156:159], v[208:211], v[90:93]
	v_mfma_f32_16x16x32_bf16 v[78:81], v[148:151], v[216:219], v[78:81]
	v_mfma_f32_16x16x32_bf16 v[74:77], v[156:159], v[216:219], v[74:77]
	v_mfma_f32_16x16x32_bf16 v[118:121], v[160:163], v[176:179], v[118:121]
	v_mfma_f32_16x16x32_bf16 v[114:117], v[168:171], v[176:179], v[114:117]
	v_mfma_f32_16x16x32_bf16 v[102:105], v[160:163], v[196:199], v[102:105]
	v_mfma_f32_16x16x32_bf16 v[98:101], v[168:171], v[196:199], v[98:101]
	v_mfma_f32_16x16x32_bf16 v[86:89], v[160:163], v[204:207], v[86:89]
	v_mfma_f32_16x16x32_bf16 v[82:85], v[168:171], v[204:207], v[82:85]
	v_mfma_f32_16x16x32_bf16 v[70:73], v[160:163], v[212:215], v[70:73]
	v_mfma_f32_16x16x32_bf16 v[66:69], v[168:171], v[212:215], v[66:69]
	v_mfma_f32_16x16x32_bf16 v[118:121], v[164:167], v[180:183], v[118:121]
	v_mfma_f32_16x16x32_bf16 v[114:117], v[172:175], v[180:183], v[114:117]
	v_mfma_f32_16x16x32_bf16 v[102:105], v[164:167], v[200:203], v[102:105]
	v_mfma_f32_16x16x32_bf16 v[98:101], v[172:175], v[200:203], v[98:101]
	v_mfma_f32_16x16x32_bf16 v[86:89], v[164:167], v[208:211], v[86:89]
	v_mfma_f32_16x16x32_bf16 v[82:85], v[172:175], v[208:211], v[82:85]
	v_mfma_f32_16x16x32_bf16 v[70:73], v[164:167], v[216:219], v[70:73]
	v_mfma_f32_16x16x32_bf16 v[66:69], v[172:175], v[216:219], v[66:69]
	s_barrier
	s_add_i32 s45, s45, s2
	v_lshl_add_u64 v[192:193], s[74:75], 0, v[186:187]
	s_mov_b32 m0, s45
	ds_read_b128 v[176:179], v142 offset:20480
	ds_read_b128 v[180:183], v142 offset:21504
	ds_read_b128 v[196:199], v142 offset:22528
	ds_read_b128 v[200:203], v142 offset:23552
	ds_read_b128 v[204:207], v142 offset:24576
	ds_read_b128 v[208:211], v142 offset:25600
	ds_read_b128 v[212:215], v142 offset:26624
	ds_read_b128 v[216:219], v142 offset:27648
	global_load_lds_dwordx4 v186, s[74:75]
	v_lshl_add_u64 v[220:221], v[192:193], 0, s[82:83]
	s_add_i32 m0, s45, 0x2000
	s_add_i32 s45, s73, s2
	global_load_lds_dwordx4 v[220:221], off
	v_lshl_add_u64 v[220:221], v[192:193], 0, s[64:65]
	s_mov_b32 m0, s45
	v_lshl_add_u64 v[184:185], s[14:15], 0, v[184:185]
	global_load_lds_dwordx4 v[220:221], off
	v_lshl_add_u64 v[220:221], v[192:193], 0, s[86:87]
	s_add_i32 m0, s45, 0x2000
	s_nop 0
	global_load_lds_dwordx4 v[220:221], off
	s_mov_b32 m0, s33
	v_lshl_add_u64 v[220:221], v[184:185], 0, s[82:83]
	global_load_lds_dwordx4 v[184:185], off
	s_mov_b32 m0, s34
	s_nop 0
	global_load_lds_dwordx4 v[220:221], off
	s_waitcnt vmcnt(8)
	s_waitcnt lgkmcnt(0)
	s_barrier
	s_waitcnt lgkmcnt(0)
	v_mfma_f32_16x16x32_bf16 v[62:65], v[144:147], v[176:179], v[62:65]
	v_mfma_f32_16x16x32_bf16 v[58:61], v[152:155], v[176:179], v[58:61]
	v_mfma_f32_16x16x32_bf16 v[46:49], v[144:147], v[196:199], v[46:49]
	v_mfma_f32_16x16x32_bf16 v[42:45], v[152:155], v[196:199], v[42:45]
	v_mfma_f32_16x16x32_bf16 v[30:33], v[144:147], v[204:207], v[30:33]
	v_mfma_f32_16x16x32_bf16 v[26:29], v[152:155], v[204:207], v[26:29]
	v_mfma_f32_16x16x32_bf16 v[14:17], v[144:147], v[212:215], v[14:17]
	v_mfma_f32_16x16x32_bf16 v[10:13], v[152:155], v[212:215], v[10:13]
	v_mfma_f32_16x16x32_bf16 v[62:65], v[148:151], v[180:183], v[62:65]
	v_mfma_f32_16x16x32_bf16 v[58:61], v[156:159], v[180:183], v[58:61]
	v_mfma_f32_16x16x32_bf16 v[46:49], v[148:151], v[200:203], v[46:49]
	v_mfma_f32_16x16x32_bf16 v[42:45], v[156:159], v[200:203], v[42:45]
	v_mfma_f32_16x16x32_bf16 v[30:33], v[148:151], v[208:211], v[30:33]
	v_mfma_f32_16x16x32_bf16 v[26:29], v[156:159], v[208:211], v[26:29]
	v_mfma_f32_16x16x32_bf16 v[14:17], v[148:151], v[216:219], v[14:17]
	v_mfma_f32_16x16x32_bf16 v[10:13], v[156:159], v[216:219], v[10:13]
	v_mfma_f32_16x16x32_bf16 v[54:57], v[160:163], v[176:179], v[54:57]
	v_mfma_f32_16x16x32_bf16 v[50:53], v[168:171], v[176:179], v[50:53]
	v_mfma_f32_16x16x32_bf16 v[38:41], v[160:163], v[196:199], v[38:41]
	v_mfma_f32_16x16x32_bf16 v[34:37], v[168:171], v[196:199], v[34:37]
	v_mfma_f32_16x16x32_bf16 v[22:25], v[160:163], v[204:207], v[22:25]
	v_mfma_f32_16x16x32_bf16 v[18:21], v[168:171], v[204:207], v[18:21]
	v_mfma_f32_16x16x32_bf16 v[6:9], v[160:163], v[212:215], v[6:9]
	v_mfma_f32_16x16x32_bf16 v[2:5], v[168:171], v[212:215], v[2:5]
	v_mfma_f32_16x16x32_bf16 v[54:57], v[164:167], v[180:183], v[54:57]
	v_mfma_f32_16x16x32_bf16 v[50:53], v[172:175], v[180:183], v[50:53]
	v_mfma_f32_16x16x32_bf16 v[38:41], v[164:167], v[200:203], v[38:41]
	v_mfma_f32_16x16x32_bf16 v[34:37], v[172:175], v[200:203], v[34:37]
	v_mfma_f32_16x16x32_bf16 v[22:25], v[164:167], v[208:211], v[22:25]
	v_mfma_f32_16x16x32_bf16 v[18:21], v[172:175], v[208:211], v[18:21]
	v_mfma_f32_16x16x32_bf16 v[6:9], v[164:167], v[216:219], v[6:9]
	v_mfma_f32_16x16x32_bf16 v[2:5], v[172:175], v[216:219], v[2:5]
	s_barrier
	s_add_i32 s14, 0, 0x19000
	v_add_u32_e32 v131, s14, v1
	s_add_i32 s15, 0, 0x1d000
	ds_read_b128 v[144:147], v131
	ds_read_b128 v[148:151], v131 offset:1024
	ds_read_b128 v[152:155], v131 offset:2048
	ds_read_b128 v[156:159], v131 offset:3072
	v_add_u32_e32 v131, s15, v1
	ds_read_b128 v[160:163], v131
	ds_read_b128 v[164:167], v131 offset:1024
	ds_read_b128 v[168:171], v131 offset:2048
	ds_read_b128 v[172:175], v131 offset:3072
	s_mov_b32 m0, s35
	v_lshl_add_u64 v[220:221], v[184:185], 0, s[64:65]
	ds_read_b128 v[176:179], v142 offset:36864
	ds_read_b128 v[180:183], v142 offset:37888
	ds_read_b128 v[196:199], v142 offset:38912
	ds_read_b128 v[200:203], v142 offset:39936
	ds_read_b128 v[204:207], v142 offset:40960
	ds_read_b128 v[208:211], v142 offset:41984
	ds_read_b128 v[212:215], v142 offset:43008
	ds_read_b128 v[216:219], v142 offset:44032
	global_load_lds_dwordx4 v[220:221], off
	v_lshl_add_u64 v[220:221], v[184:185], 0, s[86:87]
	s_mov_b32 m0, s56
	s_nop 0
	global_load_lds_dwordx4 v[220:221], off
	s_waitcnt vmcnt(8)
	s_waitcnt lgkmcnt(0)
	s_barrier
	s_waitcnt lgkmcnt(0)
	v_mfma_f32_16x16x32_bf16 v[126:129], v[144:147], v[176:179], v[126:129]
	v_mfma_f32_16x16x32_bf16 v[122:125], v[152:155], v[176:179], v[122:125]
	v_mfma_f32_16x16x32_bf16 v[110:113], v[144:147], v[196:199], v[110:113]
	v_mfma_f32_16x16x32_bf16 v[106:109], v[152:155], v[196:199], v[106:109]
	v_mfma_f32_16x16x32_bf16 v[94:97], v[144:147], v[204:207], v[94:97]
	v_mfma_f32_16x16x32_bf16 v[90:93], v[152:155], v[204:207], v[90:93]
	v_mfma_f32_16x16x32_bf16 v[78:81], v[144:147], v[212:215], v[78:81]
	v_mfma_f32_16x16x32_bf16 v[74:77], v[152:155], v[212:215], v[74:77]
	v_mfma_f32_16x16x32_bf16 v[126:129], v[148:151], v[180:183], v[126:129]
	v_mfma_f32_16x16x32_bf16 v[122:125], v[156:159], v[180:183], v[122:125]
	v_mfma_f32_16x16x32_bf16 v[110:113], v[148:151], v[200:203], v[110:113]
	v_mfma_f32_16x16x32_bf16 v[106:109], v[156:159], v[200:203], v[106:109]
	v_mfma_f32_16x16x32_bf16 v[94:97], v[148:151], v[208:211], v[94:97]
	v_mfma_f32_16x16x32_bf16 v[90:93], v[156:159], v[208:211], v[90:93]
	v_mfma_f32_16x16x32_bf16 v[78:81], v[148:151], v[216:219], v[78:81]
	v_mfma_f32_16x16x32_bf16 v[74:77], v[156:159], v[216:219], v[74:77]
	v_mfma_f32_16x16x32_bf16 v[118:121], v[160:163], v[176:179], v[118:121]
	v_mfma_f32_16x16x32_bf16 v[114:117], v[168:171], v[176:179], v[114:117]
	v_mfma_f32_16x16x32_bf16 v[102:105], v[160:163], v[196:199], v[102:105]
	v_mfma_f32_16x16x32_bf16 v[98:101], v[168:171], v[196:199], v[98:101]
	v_mfma_f32_16x16x32_bf16 v[86:89], v[160:163], v[204:207], v[86:89]
	v_mfma_f32_16x16x32_bf16 v[82:85], v[168:171], v[204:207], v[82:85]
	v_mfma_f32_16x16x32_bf16 v[70:73], v[160:163], v[212:215], v[70:73]
	v_mfma_f32_16x16x32_bf16 v[66:69], v[168:171], v[212:215], v[66:69]
	v_mfma_f32_16x16x32_bf16 v[118:121], v[164:167], v[180:183], v[118:121]
	v_mfma_f32_16x16x32_bf16 v[114:117], v[172:175], v[180:183], v[114:117]
	v_mfma_f32_16x16x32_bf16 v[102:105], v[164:167], v[200:203], v[102:105]
	v_mfma_f32_16x16x32_bf16 v[98:101], v[172:175], v[200:203], v[98:101]
	v_mfma_f32_16x16x32_bf16 v[86:89], v[164:167], v[208:211], v[86:89]
	v_mfma_f32_16x16x32_bf16 v[82:85], v[172:175], v[208:211], v[82:85]
	v_mfma_f32_16x16x32_bf16 v[70:73], v[164:167], v[216:219], v[70:73]
	v_mfma_f32_16x16x32_bf16 v[66:69], v[172:175], v[216:219], v[66:69]
	s_barrier
	s_add_i32 s14, s14, s2
	v_lshl_add_u64 v[220:221], v[192:193], 0, s[92:93]
	s_mov_b32 m0, s14
	ds_read_b128 v[176:179], v142 offset:53248
	ds_read_b128 v[180:183], v142 offset:54272
	ds_read_b128 v[196:199], v142 offset:55296
	ds_read_b128 v[200:203], v142 offset:56320
	ds_read_b128 v[204:207], v142 offset:57344
	ds_read_b128 v[208:211], v142 offset:58368
	ds_read_b128 v[212:215], v142 offset:59392
	ds_read_b128 v[216:219], v142 offset:60416
	global_load_lds_dwordx4 v[220:221], off
	v_lshl_add_u64 v[220:221], v[192:193], 0, s[4:5]
	s_add_i32 m0, s14, 0x2000
	s_add_i32 s14, s15, s2
	global_load_lds_dwordx4 v[220:221], off
	v_lshl_add_u64 v[220:221], v[192:193], 0, s[6:7]
	s_mov_b32 m0, s14
	v_lshl_add_u64 v[192:193], v[192:193], 0, s[8:9]
	global_load_lds_dwordx4 v[220:221], off
	s_add_i32 m0, s14, 0x2000
	s_nop 0
	global_load_lds_dwordx4 v[192:193], off
	v_lshl_add_u64 v[192:193], v[184:185], 0, s[92:93]
	s_mov_b32 m0, s59
	v_lshl_add_u64 v[184:185], v[184:185], 0, s[4:5]
	global_load_lds_dwordx4 v[192:193], off
	s_mov_b32 m0, s60
	s_nop 0
	global_load_lds_dwordx4 v[184:185], off
	s_waitcnt vmcnt(8)
	s_waitcnt lgkmcnt(0)
	s_barrier
	s_waitcnt lgkmcnt(0)
	v_mfma_f32_16x16x32_bf16 v[62:65], v[144:147], v[176:179], v[62:65]
	v_mfma_f32_16x16x32_bf16 v[58:61], v[152:155], v[176:179], v[58:61]
	s_add_i32 s43, s43, 2
	v_mfma_f32_16x16x32_bf16 v[46:49], v[144:147], v[196:199], v[46:49]
	s_add_u32 s54, s54, 0x100
	v_mfma_f32_16x16x32_bf16 v[42:45], v[152:155], v[196:199], v[42:45]
	s_addc_u32 s55, s55, 0
	v_mfma_f32_16x16x32_bf16 v[30:33], v[144:147], v[204:207], v[30:33]
	s_add_u32 s14, s52, s54
	v_mfma_f32_16x16x32_bf16 v[26:29], v[152:155], v[204:207], v[26:29]
	s_addc_u32 s15, s53, s55
	v_mfma_f32_16x16x32_bf16 v[14:17], v[144:147], v[212:215], v[14:17]
	s_add_u32 s45, s14, 0x100
	v_mfma_f32_16x16x32_bf16 v[10:13], v[152:155], v[212:215], v[10:13]
	s_addc_u32 s73, s15, 0
	v_mfma_f32_16x16x32_bf16 v[62:65], v[148:151], v[180:183], v[62:65]
	s_add_u32 s74, s24, s54
	v_mfma_f32_16x16x32_bf16 v[58:61], v[156:159], v[180:183], v[58:61]
	s_addc_u32 s75, s25, s55
	v_mfma_f32_16x16x32_bf16 v[46:49], v[148:151], v[200:203], v[46:49]
	s_cmpk_eq_i32 s54, 0x700
	v_mfma_f32_16x16x32_bf16 v[42:45], v[156:159], v[200:203], v[42:45]
	s_cselect_b64 vcc, -1, 0
	v_mfma_f32_16x16x32_bf16 v[30:33], v[148:151], v[208:211], v[30:33]
	s_and_b64 s[14:15], vcc, exec
	v_mfma_f32_16x16x32_bf16 v[26:29], v[156:159], v[208:211], v[26:29]
	s_cselect_b32 s15, s47, s73
	v_mfma_f32_16x16x32_bf16 v[14:17], v[148:151], v[216:219], v[14:17]
	s_cselect_b32 s14, s46, s45
	v_mfma_f32_16x16x32_bf16 v[10:13], v[156:159], v[216:219], v[10:13]
	s_cselect_b32 s75, s49, s75
	v_mfma_f32_16x16x32_bf16 v[54:57], v[160:163], v[176:179], v[54:57]
	s_cselect_b32 s74, s48, s74
	v_mfma_f32_16x16x32_bf16 v[50:53], v[168:171], v[176:179], v[50:53]
	s_add_i32 s45, 0, 0x11000
	v_mfma_f32_16x16x32_bf16 v[38:41], v[160:163], v[196:199], v[38:41]
	s_add_i32 s73, 0, 0x15000
	v_mfma_f32_16x16x32_bf16 v[34:37], v[168:171], v[196:199], v[34:37]
	v_mfma_f32_16x16x32_bf16 v[22:25], v[160:163], v[204:207], v[22:25]
	v_mfma_f32_16x16x32_bf16 v[18:21], v[168:171], v[204:207], v[18:21]
	v_mfma_f32_16x16x32_bf16 v[6:9], v[160:163], v[212:215], v[6:9]
	v_mfma_f32_16x16x32_bf16 v[2:5], v[168:171], v[212:215], v[2:5]
	v_mfma_f32_16x16x32_bf16 v[54:57], v[164:167], v[180:183], v[54:57]
	v_mfma_f32_16x16x32_bf16 v[50:53], v[172:175], v[180:183], v[50:53]
	v_mfma_f32_16x16x32_bf16 v[38:41], v[164:167], v[200:203], v[38:41]
	v_mfma_f32_16x16x32_bf16 v[34:37], v[172:175], v[200:203], v[34:37]
	v_mfma_f32_16x16x32_bf16 v[22:25], v[164:167], v[208:211], v[22:25]
	v_mfma_f32_16x16x32_bf16 v[18:21], v[172:175], v[208:211], v[18:21]
	v_mfma_f32_16x16x32_bf16 v[6:9], v[164:167], v[216:219], v[6:9]
	v_mfma_f32_16x16x32_bf16 v[2:5], v[172:175], v[216:219], v[2:5]
	s_barrier
	s_cmp_gt_u32 s43, 13
	s_cbranch_scc0 .LBB0_1111
	s_setprio 0
	s_and_b64 vcc, exec, s[40:41]
	s_cbranch_vccz .LBB0_1114
	s_barrier

.Lprio_up:
	s_add_u32 s1, s72, 0x100
	s_addc_u32 s2, s73, 0
	s_add_u32 s14, s70, 0x80
	v_mov_b32_e32 v59, v187
	v_mov_b32_e32 v65, v187
	s_addc_u32 s15, s71, 0
	v_lshl_add_u64 v[74:75], s[14:15], 0, v[64:65]
	v_lshl_add_u64 v[76:77], s[14:15], 0, v[58:59]
	s_mov_b32 s34, -2
	s_mov_b64 s[40:41], 0
	s_add_u32 s14, s70, s40
	s_addc_u32 s15, s71, s41
	s_add_u32 s35, s14, 0x100
	s_addc_u32 s55, s15, 0
	s_add_u32 s61, s1, s40
	s_addc_u32 s69, s2, s41
	s_cmpk_eq_i32 s40, 0x700
	s_cselect_b64 vcc, -1, 0
	s_and_b64 s[14:15], vcc, exec
	s_cselect_b32 s15, s59, s55
	s_cselect_b32 s14, s58, s35
	s_cselect_b32 s73, s57, s69
	s_cselect_b32 s72, s56, s61
	s_add_i32 s35, 0, 0x11000
	v_add_u32_e32 v63, s35, v165
	s_add_i32 s55, 0, 0x15000
	ds_read_b128 v[78:81], v63
	ds_read_b128 v[154:157], v63 offset:1024
	ds_read_b128 v[158:161], v63 offset:2048
	ds_read_b128 v[172:175], v63 offset:3072
	v_add_u32_e32 v63, s55, v165
	ds_read_b128 v[176:179], v63
	ds_read_b128 v[180:183], v63 offset:1024
	ds_read_b128 v[196:199], v63 offset:2048
	ds_read_b128 v[200:203], v63 offset:3072
	v_cndmask_b32_e32 v186, v62, v171, vcc
	v_cndmask_b32_e32 v184, v60, v170, vcc
	v_cndmask_b32_e32 v59, v58, v168, vcc
	v_cndmask_b32_e32 v61, v64, v169, vcc
	v_lshl_add_u64 v[192:193], v[76:77], 0, s[40:41]
	s_add_i32 m0, s24, 0xd000
	ds_read_b128 v[204:207], v166 offset:4096
	ds_read_b128 v[208:211], v166 offset:5120
	ds_read_b128 v[212:215], v166 offset:6144
	ds_read_b128 v[216:219], v166 offset:7168
	ds_read_b128 v[220:223], v166 offset:8192
	ds_read_b128 v[240:243], v166 offset:9216
	ds_read_b128 v[244:247], v166 offset:10240
	ds_read_b128 v[248:251], v166 offset:11264
	global_load_lds_dwordx4 v[192:193], off
	v_lshl_add_u64 v[192:193], v[74:75], 0, s[40:41]
	s_add_i32 m0, s24, 0xf000
	s_nop 0
	global_load_lds_dwordx4 v[192:193], off
	s_waitcnt vmcnt(8)
	s_waitcnt lgkmcnt(0)
	s_barrier
	s_waitcnt lgkmcnt(0)
	v_mfma_f32_16x16x32_bf16 v[142:145], v[78:81], v[204:207], 0
	v_mfma_f32_16x16x32_bf16 v[134:137], v[158:161], v[204:207], 0
	v_mfma_f32_16x16x32_bf16 v[126:129], v[78:81], v[212:215], 0
	v_mfma_f32_16x16x32_bf16 v[118:121], v[158:161], v[212:215], 0
	v_mfma_f32_16x16x32_bf16 v[110:113], v[78:81], v[220:223], 0
	v_mfma_f32_16x16x32_bf16 v[102:105], v[158:161], v[220:223], 0
	v_mfma_f32_16x16x32_bf16 v[94:97], v[78:81], v[244:247], 0
	v_mfma_f32_16x16x32_bf16 v[86:89], v[158:161], v[244:247], 0
	v_mfma_f32_16x16x32_bf16 v[142:145], v[154:157], v[208:211], v[142:145]
	v_mfma_f32_16x16x32_bf16 v[134:137], v[172:175], v[208:211], v[134:137]
	v_mfma_f32_16x16x32_bf16 v[126:129], v[154:157], v[216:219], v[126:129]
	v_mfma_f32_16x16x32_bf16 v[118:121], v[172:175], v[216:219], v[118:121]
	v_mfma_f32_16x16x32_bf16 v[110:113], v[154:157], v[240:243], v[110:113]
	v_mfma_f32_16x16x32_bf16 v[102:105], v[172:175], v[240:243], v[102:105]
	v_mfma_f32_16x16x32_bf16 v[94:97], v[154:157], v[248:251], v[94:97]
	v_mfma_f32_16x16x32_bf16 v[86:89], v[172:175], v[248:251], v[86:89]
	v_mfma_f32_16x16x32_bf16 v[138:141], v[176:179], v[204:207], 0
	v_mfma_f32_16x16x32_bf16 v[130:133], v[196:199], v[204:207], 0
	v_mfma_f32_16x16x32_bf16 v[122:125], v[176:179], v[212:215], 0
	v_mfma_f32_16x16x32_bf16 v[114:117], v[196:199], v[212:215], 0
	v_mfma_f32_16x16x32_bf16 v[106:109], v[176:179], v[220:223], 0
	v_mfma_f32_16x16x32_bf16 v[98:101], v[196:199], v[220:223], 0
	v_mfma_f32_16x16x32_bf16 v[90:93], v[176:179], v[244:247], 0
	v_mfma_f32_16x16x32_bf16 v[82:85], v[196:199], v[244:247], 0
	v_mfma_f32_16x16x32_bf16 v[138:141], v[180:183], v[208:211], v[138:141]
	v_mfma_f32_16x16x32_bf16 v[130:133], v[200:203], v[208:211], v[130:133]
	v_mfma_f32_16x16x32_bf16 v[122:125], v[180:183], v[216:219], v[122:125]
	v_mfma_f32_16x16x32_bf16 v[114:117], v[200:203], v[216:219], v[114:117]
	v_mfma_f32_16x16x32_bf16 v[106:109], v[180:183], v[240:243], v[106:109]
	v_mfma_f32_16x16x32_bf16 v[98:101], v[200:203], v[240:243], v[98:101]
	v_mfma_f32_16x16x32_bf16 v[90:93], v[180:183], v[248:251], v[90:93]
	v_mfma_f32_16x16x32_bf16 v[82:85], v[200:203], v[248:251], v[82:85]
	s_barrier
	s_add_i32 s35, s35, s17
	v_lshl_add_u64 v[192:193], s[72:73], 0, v[148:149]
	s_mov_b32 m0, s35
	ds_read_b128 v[204:207], v166 offset:20480
	ds_read_b128 v[208:211], v166 offset:21504
	ds_read_b128 v[212:215], v166 offset:22528
	ds_read_b128 v[216:219], v166 offset:23552
	ds_read_b128 v[220:223], v166 offset:24576
	ds_read_b128 v[240:243], v166 offset:25600
	ds_read_b128 v[244:247], v166 offset:26624
	ds_read_b128 v[248:251], v166 offset:27648
	global_load_lds_dwordx4 v[192:193], off
	v_lshl_add_u64 v[224:225], v[192:193], 0, s[82:83]
	s_add_i32 m0, s35, 0x2000
	s_add_i32 s35, s55, s17
	global_load_lds_dwordx4 v[224:225], off
	v_lshl_add_u64 v[224:225], v[192:193], 0, s[64:65]
	s_mov_b32 m0, s35
	v_mov_b32_e32 v185, v187
	global_load_lds_dwordx4 v[224:225], off
	v_lshl_add_u64 v[224:225], v[192:193], 0, s[86:87]
	s_add_i32 m0, s35, 0x2000
	s_nop 0
	global_load_lds_dwordx4 v[224:225], off
	s_mov_b32 m0, s25
	v_lshl_add_u64 v[224:225], s[14:15], 0, v[186:187]
	global_load_lds_dwordx4 v186, s[14:15]
	s_mov_b32 m0, s28
	s_nop 0
	global_load_lds_dwordx4 v184, s[14:15]
	s_waitcnt vmcnt(8)
	s_waitcnt lgkmcnt(0)
	v_lshl_add_u64 v[184:185], s[14:15], 0, v[184:185]
	s_barrier
	s_cmp_lg_u64 s[38:39], 0
	s_cbranch_scc1 .Lup_tokskip
	v_lshlrev_b32_e32 v2, 10, v2
	v_lshlrev_b32_e32 v3, 10, v3
	v_lshlrev_b32_e32 v5, 10, v5
	v_lshlrev_b32_e32 v4, 10, v4
	v_add_lshl_u32 v168, v5, v164, 1
	v_add_lshl_u32 v170, v3, v164, 1
	v_add_lshl_u32 v171, v2, v164, 1
	v_add_lshl_u32 v169, v4, v164, 1
.Lup_tokskip:
	s_waitcnt lgkmcnt(0)
	v_mfma_f32_16x16x32_bf16 v[70:73], v[78:81], v[204:207], 0
	v_mfma_f32_16x16x32_bf16 v[54:57], v[158:161], v[204:207], 0
	v_mfma_f32_16x16x32_bf16 v[46:49], v[78:81], v[212:215], 0
	v_mfma_f32_16x16x32_bf16 v[38:41], v[158:161], v[212:215], 0
	v_mfma_f32_16x16x32_bf16 v[30:33], v[78:81], v[220:223], 0
	v_mfma_f32_16x16x32_bf16 v[22:25], v[158:161], v[220:223], 0
	v_mfma_f32_16x16x32_bf16 v[14:17], v[78:81], v[244:247], 0
	v_mfma_f32_16x16x32_bf16 v[6:9], v[158:161], v[244:247], 0
	v_mfma_f32_16x16x32_bf16 v[70:73], v[154:157], v[208:211], v[70:73]
	v_mfma_f32_16x16x32_bf16 v[54:57], v[172:175], v[208:211], v[54:57]
	v_mfma_f32_16x16x32_bf16 v[46:49], v[154:157], v[216:219], v[46:49]
	v_mfma_f32_16x16x32_bf16 v[38:41], v[172:175], v[216:219], v[38:41]
	v_mfma_f32_16x16x32_bf16 v[30:33], v[154:157], v[240:243], v[30:33]
	v_mfma_f32_16x16x32_bf16 v[22:25], v[172:175], v[240:243], v[22:25]
	v_mfma_f32_16x16x32_bf16 v[14:17], v[154:157], v[248:251], v[14:17]
	v_mfma_f32_16x16x32_bf16 v[6:9], v[172:175], v[248:251], v[6:9]
	v_mfma_f32_16x16x32_bf16 v[66:69], v[176:179], v[204:207], 0
	v_mfma_f32_16x16x32_bf16 v[50:53], v[196:199], v[204:207], 0
	v_mfma_f32_16x16x32_bf16 v[42:45], v[176:179], v[212:215], 0
	v_mfma_f32_16x16x32_bf16 v[34:37], v[196:199], v[212:215], 0
	v_mfma_f32_16x16x32_bf16 v[26:29], v[176:179], v[220:223], 0
	v_mfma_f32_16x16x32_bf16 v[18:21], v[196:199], v[220:223], 0
	v_mfma_f32_16x16x32_bf16 v[10:13], v[176:179], v[244:247], 0
	v_mfma_f32_16x16x32_bf16 v[2:5], v[196:199], v[244:247], 0
	v_mfma_f32_16x16x32_bf16 v[66:69], v[180:183], v[208:211], v[66:69]
	v_mfma_f32_16x16x32_bf16 v[50:53], v[200:203], v[208:211], v[50:53]
	v_mfma_f32_16x16x32_bf16 v[42:45], v[180:183], v[216:219], v[42:45]
	v_mfma_f32_16x16x32_bf16 v[34:37], v[200:203], v[216:219], v[34:37]
	v_mfma_f32_16x16x32_bf16 v[26:29], v[180:183], v[240:243], v[26:29]
	v_mfma_f32_16x16x32_bf16 v[18:21], v[200:203], v[240:243], v[18:21]
	v_mfma_f32_16x16x32_bf16 v[10:13], v[180:183], v[248:251], v[10:13]
	v_mfma_f32_16x16x32_bf16 v[2:5], v[200:203], v[248:251], v[2:5]
	s_barrier
	s_add_i32 s35, 0, 0x19000
	v_add_u32_e32 v63, s35, v165
	s_add_i32 s55, 0, 0x1d000
	ds_read_b128 v[78:81], v63
	ds_read_b128 v[154:157], v63 offset:1024
	ds_read_b128 v[158:161], v63 offset:2048
	ds_read_b128 v[172:175], v63 offset:3072
	v_add_u32_e32 v63, s55, v165
	ds_read_b128 v[176:179], v63
	ds_read_b128 v[180:183], v63 offset:1024
	ds_read_b128 v[196:199], v63 offset:2048
	ds_read_b128 v[200:203], v63 offset:3072
	s_mov_b32 m0, s29
	ds_read_b128 v[204:207], v166 offset:36864
	ds_read_b128 v[208:211], v166 offset:37888
	ds_read_b128 v[212:215], v166 offset:38912
	ds_read_b128 v[216:219], v166 offset:39936
	ds_read_b128 v[220:223], v166 offset:40960
	ds_read_b128 v[240:243], v166 offset:41984
	ds_read_b128 v[244:247], v166 offset:43008
	ds_read_b128 v[248:251], v166 offset:44032
	global_load_lds_dwordx4 v59, s[14:15]
	s_mov_b32 m0, s33
	s_nop 0
	global_load_lds_dwordx4 v61, s[14:15]
	s_waitcnt vmcnt(8)
	s_waitcnt lgkmcnt(0)
	s_barrier
	s_waitcnt lgkmcnt(0)
	v_mfma_f32_16x16x32_bf16 v[142:145], v[78:81], v[204:207], v[142:145]
	v_mfma_f32_16x16x32_bf16 v[134:137], v[158:161], v[204:207], v[134:137]
	v_mfma_f32_16x16x32_bf16 v[126:129], v[78:81], v[212:215], v[126:129]
	v_mfma_f32_16x16x32_bf16 v[118:121], v[158:161], v[212:215], v[118:121]
	v_mfma_f32_16x16x32_bf16 v[110:113], v[78:81], v[220:223], v[110:113]
	v_mfma_f32_16x16x32_bf16 v[102:105], v[158:161], v[220:223], v[102:105]
	v_mfma_f32_16x16x32_bf16 v[94:97], v[78:81], v[244:247], v[94:97]
	v_mfma_f32_16x16x32_bf16 v[86:89], v[158:161], v[244:247], v[86:89]
	v_mfma_f32_16x16x32_bf16 v[142:145], v[154:157], v[208:211], v[142:145]
	v_mfma_f32_16x16x32_bf16 v[134:137], v[172:175], v[208:211], v[134:137]
	v_mfma_f32_16x16x32_bf16 v[126:129], v[154:157], v[216:219], v[126:129]
	v_mfma_f32_16x16x32_bf16 v[118:121], v[172:175], v[216:219], v[118:121]
	v_mfma_f32_16x16x32_bf16 v[110:113], v[154:157], v[240:243], v[110:113]
	v_mfma_f32_16x16x32_bf16 v[102:105], v[172:175], v[240:243], v[102:105]
	v_mfma_f32_16x16x32_bf16 v[94:97], v[154:157], v[248:251], v[94:97]
	v_mfma_f32_16x16x32_bf16 v[86:89], v[172:175], v[248:251], v[86:89]
	v_mfma_f32_16x16x32_bf16 v[138:141], v[176:179], v[204:207], v[138:141]
	v_mfma_f32_16x16x32_bf16 v[130:133], v[196:199], v[204:207], v[130:133]
	v_mfma_f32_16x16x32_bf16 v[122:125], v[176:179], v[212:215], v[122:125]
	v_mfma_f32_16x16x32_bf16 v[114:117], v[196:199], v[212:215], v[114:117]
	v_mfma_f32_16x16x32_bf16 v[106:109], v[176:179], v[220:223], v[106:109]
	v_mfma_f32_16x16x32_bf16 v[98:101], v[196:199], v[220:223], v[98:101]
	v_mfma_f32_16x16x32_bf16 v[90:93], v[176:179], v[244:247], v[90:93]
	v_mfma_f32_16x16x32_bf16 v[82:85], v[196:199], v[244:247], v[82:85]
	v_mfma_f32_16x16x32_bf16 v[138:141], v[180:183], v[208:211], v[138:141]
	v_mfma_f32_16x16x32_bf16 v[130:133], v[200:203], v[208:211], v[130:133]
	v_mfma_f32_16x16x32_bf16 v[122:125], v[180:183], v[216:219], v[122:125]
	v_mfma_f32_16x16x32_bf16 v[114:117], v[200:203], v[216:219], v[114:117]
	v_mfma_f32_16x16x32_bf16 v[106:109], v[180:183], v[240:243], v[106:109]
	v_mfma_f32_16x16x32_bf16 v[98:101], v[200:203], v[240:243], v[98:101]
	v_mfma_f32_16x16x32_bf16 v[90:93], v[180:183], v[248:251], v[90:93]
	v_mfma_f32_16x16x32_bf16 v[82:85], v[200:203], v[248:251], v[82:85]
	s_barrier
	s_add_i32 s14, s35, s17
	v_lshl_add_u64 v[230:231], v[192:193], 0, s[92:93]
	s_mov_b32 m0, s14
	ds_read_b128 v[204:207], v166 offset:53248
	ds_read_b128 v[208:211], v166 offset:54272
	ds_read_b128 v[212:215], v166 offset:55296
	ds_read_b128 v[216:219], v166 offset:56320
	ds_read_b128 v[220:223], v166 offset:57344
	ds_read_b128 v[240:243], v166 offset:58368
	ds_read_b128 v[244:247], v166 offset:59392
	ds_read_b128 v[248:251], v166 offset:60416
	global_load_lds_dwordx4 v[230:231], off
	v_lshl_add_u64 v[230:231], v[192:193], 0, s[4:5]
	s_add_i32 m0, s14, 0x2000
	s_add_i32 s14, s55, s17
	global_load_lds_dwordx4 v[230:231], off
	v_lshl_add_u64 v[230:231], v[192:193], 0, s[6:7]
	s_mov_b32 m0, s14
	v_lshl_add_u64 v[192:193], v[192:193], 0, s[8:9]
	global_load_lds_dwordx4 v[230:231], off
	s_add_i32 m0, s14, 0x2000
	v_lshl_add_u64 v[184:185], v[184:185], 0, s[92:93]
	global_load_lds_dwordx4 v[192:193], off
	v_lshl_add_u64 v[192:193], v[224:225], 0, s[92:93]
	s_mov_b32 m0, s80
	s_nop 0
	global_load_lds_dwordx4 v[192:193], off
	s_mov_b32 m0, s81
	s_nop 0
	global_load_lds_dwordx4 v[184:185], off
	s_waitcnt vmcnt(8)
	s_waitcnt lgkmcnt(0)
	s_barrier
	s_waitcnt lgkmcnt(0)
	v_mfma_f32_16x16x32_bf16 v[70:73], v[78:81], v[204:207], v[70:73]
	v_mfma_f32_16x16x32_bf16 v[54:57], v[158:161], v[204:207], v[54:57]
	s_add_i32 s34, s34, 2
	v_mfma_f32_16x16x32_bf16 v[46:49], v[78:81], v[212:215], v[46:49]
	s_add_u32 s40, s40, 0x100
	v_mfma_f32_16x16x32_bf16 v[38:41], v[158:161], v[212:215], v[38:41]
	s_addc_u32 s41, s41, 0
	v_mfma_f32_16x16x32_bf16 v[30:33], v[78:81], v[220:223], v[30:33]
	s_add_u32 s14, s70, s40
	v_mfma_f32_16x16x32_bf16 v[22:25], v[158:161], v[220:223], v[22:25]
	s_addc_u32 s15, s71, s41
	v_mfma_f32_16x16x32_bf16 v[14:17], v[78:81], v[244:247], v[14:17]
	s_add_u32 s35, s14, 0x100
	v_mfma_f32_16x16x32_bf16 v[6:9], v[158:161], v[244:247], v[6:9]
	s_addc_u32 s55, s15, 0
	v_mfma_f32_16x16x32_bf16 v[70:73], v[154:157], v[208:211], v[70:73]
	s_add_u32 s61, s1, s40
	v_mfma_f32_16x16x32_bf16 v[54:57], v[172:175], v[208:211], v[54:57]
	s_addc_u32 s69, s2, s41
	v_mfma_f32_16x16x32_bf16 v[46:49], v[154:157], v[216:219], v[46:49]
	s_cmpk_eq_i32 s40, 0x700
	v_mfma_f32_16x16x32_bf16 v[38:41], v[172:175], v[216:219], v[38:41]
	s_cselect_b64 vcc, -1, 0
	v_mfma_f32_16x16x32_bf16 v[30:33], v[154:157], v[240:243], v[30:33]
	s_and_b64 s[14:15], vcc, exec
	v_mfma_f32_16x16x32_bf16 v[22:25], v[172:175], v[240:243], v[22:25]
	s_cselect_b32 s15, s59, s55
	v_mfma_f32_16x16x32_bf16 v[14:17], v[154:157], v[248:251], v[14:17]
	s_cselect_b32 s14, s58, s35
	v_mfma_f32_16x16x32_bf16 v[6:9], v[172:175], v[248:251], v[6:9]
	s_cselect_b32 s73, s57, s69
	v_mfma_f32_16x16x32_bf16 v[66:69], v[176:179], v[204:207], v[66:69]
	s_cselect_b32 s72, s56, s61
	v_mfma_f32_16x16x32_bf16 v[50:53], v[196:199], v[204:207], v[50:53]
	s_add_i32 s35, 0, 0x11000
	v_mfma_f32_16x16x32_bf16 v[42:45], v[176:179], v[212:215], v[42:45]
	s_add_i32 s55, 0, 0x15000
	v_mfma_f32_16x16x32_bf16 v[34:37], v[196:199], v[212:215], v[34:37]
	v_mfma_f32_16x16x32_bf16 v[26:29], v[176:179], v[220:223], v[26:29]
	v_mfma_f32_16x16x32_bf16 v[18:21], v[196:199], v[220:223], v[18:21]
	v_mfma_f32_16x16x32_bf16 v[10:13], v[176:179], v[244:247], v[10:13]
	v_mfma_f32_16x16x32_bf16 v[2:5], v[196:199], v[244:247], v[2:5]
	v_mfma_f32_16x16x32_bf16 v[66:69], v[180:183], v[208:211], v[66:69]
	v_mfma_f32_16x16x32_bf16 v[50:53], v[200:203], v[208:211], v[50:53]
	v_mfma_f32_16x16x32_bf16 v[42:45], v[180:183], v[216:219], v[42:45]
	v_mfma_f32_16x16x32_bf16 v[34:37], v[200:203], v[216:219], v[34:37]
	v_mfma_f32_16x16x32_bf16 v[26:29], v[180:183], v[240:243], v[26:29]
	v_mfma_f32_16x16x32_bf16 v[18:21], v[200:203], v[240:243], v[18:21]
	v_mfma_f32_16x16x32_bf16 v[10:13], v[180:183], v[248:251], v[10:13]
	v_mfma_f32_16x16x32_bf16 v[2:5], v[200:203], v[248:251], v[2:5]
	s_barrier
.LBB0_1339:
	v_add_u32_e32 v63, s35, v165
	ds_read_b128 v[78:81], v63
	ds_read_b128 v[154:157], v63 offset:1024
	ds_read_b128 v[158:161], v63 offset:2048
	ds_read_b128 v[172:175], v63 offset:3072
	v_add_u32_e32 v63, s55, v165
	ds_read_b128 v[176:179], v63
	ds_read_b128 v[180:183], v63 offset:1024
	ds_read_b128 v[196:199], v63 offset:2048
	ds_read_b128 v[200:203], v63 offset:3072
	v_cndmask_b32_e32 v186, v62, v171, vcc
	v_cndmask_b32_e32 v184, v60, v170, vcc
	v_cndmask_b32_e32 v59, v58, v168, vcc
	v_cndmask_b32_e32 v61, v64, v169, vcc
	v_lshl_add_u64 v[192:193], v[76:77], 0, s[40:41]
	s_add_i32 m0, s24, 0xd000
	ds_read_b128 v[204:207], v166 offset:4096
	ds_read_b128 v[208:211], v166 offset:5120
	ds_read_b128 v[212:215], v166 offset:6144
	ds_read_b128 v[216:219], v166 offset:7168
	ds_read_b128 v[220:223], v166 offset:8192
	ds_read_b128 v[240:243], v166 offset:9216
	ds_read_b128 v[244:247], v166 offset:10240
	ds_read_b128 v[248:251], v166 offset:11264
	global_load_lds_dwordx4 v[192:193], off
	v_lshl_add_u64 v[192:193], v[74:75], 0, s[40:41]
	s_add_i32 m0, s24, 0xf000
	s_nop 0
	global_load_lds_dwordx4 v[192:193], off
	s_waitcnt vmcnt(8)
	s_waitcnt lgkmcnt(0)
	s_barrier
	s_waitcnt lgkmcnt(0)
	v_mfma_f32_16x16x32_bf16 v[142:145], v[78:81], v[204:207], v[142:145]
	v_mfma_f32_16x16x32_bf16 v[134:137], v[158:161], v[204:207], v[134:137]
	v_mfma_f32_16x16x32_bf16 v[126:129], v[78:81], v[212:215], v[126:129]
	v_mfma_f32_16x16x32_bf16 v[118:121], v[158:161], v[212:215], v[118:121]
	v_mfma_f32_16x16x32_bf16 v[110:113], v[78:81], v[220:223], v[110:113]
	v_mfma_f32_16x16x32_bf16 v[102:105], v[158:161], v[220:223], v[102:105]
	v_mfma_f32_16x16x32_bf16 v[94:97], v[78:81], v[244:247], v[94:97]
	v_mfma_f32_16x16x32_bf16 v[86:89], v[158:161], v[244:247], v[86:89]
	v_mfma_f32_16x16x32_bf16 v[142:145], v[154:157], v[208:211], v[142:145]
	v_mfma_f32_16x16x32_bf16 v[134:137], v[172:175], v[208:211], v[134:137]
	v_mfma_f32_16x16x32_bf16 v[126:129], v[154:157], v[216:219], v[126:129]
	v_mfma_f32_16x16x32_bf16 v[118:121], v[172:175], v[216:219], v[118:121]
	v_mfma_f32_16x16x32_bf16 v[110:113], v[154:157], v[240:243], v[110:113]
	v_mfma_f32_16x16x32_bf16 v[102:105], v[172:175], v[240:243], v[102:105]
	v_mfma_f32_16x16x32_bf16 v[94:97], v[154:157], v[248:251], v[94:97]
	v_mfma_f32_16x16x32_bf16 v[86:89], v[172:175], v[248:251], v[86:89]
	v_mfma_f32_16x16x32_bf16 v[138:141], v[176:179], v[204:207], v[138:141]
	v_mfma_f32_16x16x32_bf16 v[130:133], v[196:199], v[204:207], v[130:133]
	v_mfma_f32_16x16x32_bf16 v[122:125], v[176:179], v[212:215], v[122:125]
	v_mfma_f32_16x16x32_bf16 v[114:117], v[196:199], v[212:215], v[114:117]
	v_mfma_f32_16x16x32_bf16 v[106:109], v[176:179], v[220:223], v[106:109]
	v_mfma_f32_16x16x32_bf16 v[98:101], v[196:199], v[220:223], v[98:101]
	v_mfma_f32_16x16x32_bf16 v[90:93], v[176:179], v[244:247], v[90:93]
	v_mfma_f32_16x16x32_bf16 v[82:85], v[196:199], v[244:247], v[82:85]
	v_mfma_f32_16x16x32_bf16 v[138:141], v[180:183], v[208:211], v[138:141]
	v_mfma_f32_16x16x32_bf16 v[130:133], v[200:203], v[208:211], v[130:133]
	v_mfma_f32_16x16x32_bf16 v[122:125], v[180:183], v[216:219], v[122:125]
	v_mfma_f32_16x16x32_bf16 v[114:117], v[200:203], v[216:219], v[114:117]
	v_mfma_f32_16x16x32_bf16 v[106:109], v[180:183], v[240:243], v[106:109]
	v_mfma_f32_16x16x32_bf16 v[98:101], v[200:203], v[240:243], v[98:101]
	v_mfma_f32_16x16x32_bf16 v[90:93], v[180:183], v[248:251], v[90:93]
	v_mfma_f32_16x16x32_bf16 v[82:85], v[200:203], v[248:251], v[82:85]
	s_barrier
	s_add_i32 s35, s35, s17
	v_lshl_add_u64 v[192:193], s[72:73], 0, v[148:149]
	s_mov_b32 m0, s35
	ds_read_b128 v[204:207], v166 offset:20480
	ds_read_b128 v[208:211], v166 offset:21504
	ds_read_b128 v[212:215], v166 offset:22528
	ds_read_b128 v[216:219], v166 offset:23552
	ds_read_b128 v[220:223], v166 offset:24576
	ds_read_b128 v[240:243], v166 offset:25600
	ds_read_b128 v[244:247], v166 offset:26624
	ds_read_b128 v[248:251], v166 offset:27648
	global_load_lds_dwordx4 v[192:193], off
	v_lshl_add_u64 v[224:225], v[192:193], 0, s[82:83]
	s_add_i32 m0, s35, 0x2000
	s_add_i32 s35, s55, s17
	global_load_lds_dwordx4 v[224:225], off
	v_lshl_add_u64 v[224:225], v[192:193], 0, s[64:65]
	s_mov_b32 m0, s35
	v_mov_b32_e32 v185, v187
	global_load_lds_dwordx4 v[224:225], off
	v_lshl_add_u64 v[224:225], v[192:193], 0, s[86:87]
	s_add_i32 m0, s35, 0x2000
	s_nop 0
	global_load_lds_dwordx4 v[224:225], off
	s_mov_b32 m0, s25
	v_lshl_add_u64 v[224:225], s[14:15], 0, v[186:187]
	global_load_lds_dwordx4 v186, s[14:15]
	s_mov_b32 m0, s28
	s_nop 0
	global_load_lds_dwordx4 v184, s[14:15]
	s_waitcnt vmcnt(8)
	s_waitcnt lgkmcnt(0)
	v_lshl_add_u64 v[184:185], s[14:15], 0, v[184:185]
	s_barrier
	s_waitcnt lgkmcnt(0)
	v_mfma_f32_16x16x32_bf16 v[70:73], v[78:81], v[204:207], v[70:73]
	v_mfma_f32_16x16x32_bf16 v[54:57], v[158:161], v[204:207], v[54:57]
	v_mfma_f32_16x16x32_bf16 v[46:49], v[78:81], v[212:215], v[46:49]
	v_mfma_f32_16x16x32_bf16 v[38:41], v[158:161], v[212:215], v[38:41]
	v_mfma_f32_16x16x32_bf16 v[30:33], v[78:81], v[220:223], v[30:33]
	v_mfma_f32_16x16x32_bf16 v[22:25], v[158:161], v[220:223], v[22:25]
	v_mfma_f32_16x16x32_bf16 v[14:17], v[78:81], v[244:247], v[14:17]
	v_mfma_f32_16x16x32_bf16 v[6:9], v[158:161], v[244:247], v[6:9]
	v_mfma_f32_16x16x32_bf16 v[70:73], v[154:157], v[208:211], v[70:73]
	v_mfma_f32_16x16x32_bf16 v[54:57], v[172:175], v[208:211], v[54:57]
	v_mfma_f32_16x16x32_bf16 v[46:49], v[154:157], v[216:219], v[46:49]
	v_mfma_f32_16x16x32_bf16 v[38:41], v[172:175], v[216:219], v[38:41]
	v_mfma_f32_16x16x32_bf16 v[30:33], v[154:157], v[240:243], v[30:33]
	v_mfma_f32_16x16x32_bf16 v[22:25], v[172:175], v[240:243], v[22:25]
	v_mfma_f32_16x16x32_bf16 v[14:17], v[154:157], v[248:251], v[14:17]
	v_mfma_f32_16x16x32_bf16 v[6:9], v[172:175], v[248:251], v[6:9]
	v_mfma_f32_16x16x32_bf16 v[66:69], v[176:179], v[204:207], v[66:69]
	v_mfma_f32_16x16x32_bf16 v[50:53], v[196:199], v[204:207], v[50:53]
	v_mfma_f32_16x16x32_bf16 v[42:45], v[176:179], v[212:215], v[42:45]
	v_mfma_f32_16x16x32_bf16 v[34:37], v[196:199], v[212:215], v[34:37]
	v_mfma_f32_16x16x32_bf16 v[26:29], v[176:179], v[220:223], v[26:29]
	v_mfma_f32_16x16x32_bf16 v[18:21], v[196:199], v[220:223], v[18:21]
	v_mfma_f32_16x16x32_bf16 v[10:13], v[176:179], v[244:247], v[10:13]
	v_mfma_f32_16x16x32_bf16 v[2:5], v[196:199], v[244:247], v[2:5]
	v_mfma_f32_16x16x32_bf16 v[66:69], v[180:183], v[208:211], v[66:69]
	v_mfma_f32_16x16x32_bf16 v[50:53], v[200:203], v[208:211], v[50:53]
	v_mfma_f32_16x16x32_bf16 v[42:45], v[180:183], v[216:219], v[42:45]
	v_mfma_f32_16x16x32_bf16 v[34:37], v[200:203], v[216:219], v[34:37]
	v_mfma_f32_16x16x32_bf16 v[26:29], v[180:183], v[240:243], v[26:29]
	v_mfma_f32_16x16x32_bf16 v[18:21], v[200:203], v[240:243], v[18:21]
	v_mfma_f32_16x16x32_bf16 v[10:13], v[180:183], v[248:251], v[10:13]
	v_mfma_f32_16x16x32_bf16 v[2:5], v[200:203], v[248:251], v[2:5]
	s_barrier
	s_add_i32 s35, 0, 0x19000
	v_add_u32_e32 v63, s35, v165
	s_add_i32 s55, 0, 0x1d000
	ds_read_b128 v[78:81], v63
	ds_read_b128 v[154:157], v63 offset:1024
	ds_read_b128 v[158:161], v63 offset:2048
	ds_read_b128 v[172:175], v63 offset:3072
	v_add_u32_e32 v63, s55, v165
	ds_read_b128 v[176:179], v63
	ds_read_b128 v[180:183], v63 offset:1024
	ds_read_b128 v[196:199], v63 offset:2048
	ds_read_b128 v[200:203], v63 offset:3072
	s_mov_b32 m0, s29
	ds_read_b128 v[204:207], v166 offset:36864
	ds_read_b128 v[208:211], v166 offset:37888
	ds_read_b128 v[212:215], v166 offset:38912
	ds_read_b128 v[216:219], v166 offset:39936
	ds_read_b128 v[220:223], v166 offset:40960
	ds_read_b128 v[240:243], v166 offset:41984
	ds_read_b128 v[244:247], v166 offset:43008
	ds_read_b128 v[248:251], v166 offset:44032
	global_load_lds_dwordx4 v59, s[14:15]
	s_mov_b32 m0, s33
	s_nop 0
	global_load_lds_dwordx4 v61, s[14:15]
	s_waitcnt vmcnt(8)
	s_waitcnt lgkmcnt(0)
	s_barrier
	s_waitcnt lgkmcnt(0)
	v_mfma_f32_16x16x32_bf16 v[142:145], v[78:81], v[204:207], v[142:145]
	v_mfma_f32_16x16x32_bf16 v[134:137], v[158:161], v[204:207], v[134:137]
	v_mfma_f32_16x16x32_bf16 v[126:129], v[78:81], v[212:215], v[126:129]
	v_mfma_f32_16x16x32_bf16 v[118:121], v[158:161], v[212:215], v[118:121]
	v_mfma_f32_16x16x32_bf16 v[110:113], v[78:81], v[220:223], v[110:113]
	v_mfma_f32_16x16x32_bf16 v[102:105], v[158:161], v[220:223], v[102:105]
	v_mfma_f32_16x16x32_bf16 v[94:97], v[78:81], v[244:247], v[94:97]
	v_mfma_f32_16x16x32_bf16 v[86:89], v[158:161], v[244:247], v[86:89]
	v_mfma_f32_16x16x32_bf16 v[142:145], v[154:157], v[208:211], v[142:145]
	v_mfma_f32_16x16x32_bf16 v[134:137], v[172:175], v[208:211], v[134:137]
	v_mfma_f32_16x16x32_bf16 v[126:129], v[154:157], v[216:219], v[126:129]
	v_mfma_f32_16x16x32_bf16 v[118:121], v[172:175], v[216:219], v[118:121]
	v_mfma_f32_16x16x32_bf16 v[110:113], v[154:157], v[240:243], v[110:113]
	v_mfma_f32_16x16x32_bf16 v[102:105], v[172:175], v[240:243], v[102:105]
	v_mfma_f32_16x16x32_bf16 v[94:97], v[154:157], v[248:251], v[94:97]
	v_mfma_f32_16x16x32_bf16 v[86:89], v[172:175], v[248:251], v[86:89]
	v_mfma_f32_16x16x32_bf16 v[138:141], v[176:179], v[204:207], v[138:141]
	v_mfma_f32_16x16x32_bf16 v[130:133], v[196:199], v[204:207], v[130:133]
	v_mfma_f32_16x16x32_bf16 v[122:125], v[176:179], v[212:215], v[122:125]
	v_mfma_f32_16x16x32_bf16 v[114:117], v[196:199], v[212:215], v[114:117]
	v_mfma_f32_16x16x32_bf16 v[106:109], v[176:179], v[220:223], v[106:109]
	v_mfma_f32_16x16x32_bf16 v[98:101], v[196:199], v[220:223], v[98:101]
	v_mfma_f32_16x16x32_bf16 v[90:93], v[176:179], v[244:247], v[90:93]
	v_mfma_f32_16x16x32_bf16 v[82:85], v[196:199], v[244:247], v[82:85]
	v_mfma_f32_16x16x32_bf16 v[138:141], v[180:183], v[208:211], v[138:141]
	v_mfma_f32_16x16x32_bf16 v[130:133], v[200:203], v[208:211], v[130:133]
	v_mfma_f32_16x16x32_bf16 v[122:125], v[180:183], v[216:219], v[122:125]
	v_mfma_f32_16x16x32_bf16 v[114:117], v[200:203], v[216:219], v[114:117]
	v_mfma_f32_16x16x32_bf16 v[106:109], v[180:183], v[240:243], v[106:109]
	v_mfma_f32_16x16x32_bf16 v[98:101], v[200:203], v[240:243], v[98:101]
	v_mfma_f32_16x16x32_bf16 v[90:93], v[180:183], v[248:251], v[90:93]
	v_mfma_f32_16x16x32_bf16 v[82:85], v[200:203], v[248:251], v[82:85]
	s_barrier
	s_add_i32 s14, s35, s17
	v_lshl_add_u64 v[230:231], v[192:193], 0, s[92:93]
	s_mov_b32 m0, s14
	ds_read_b128 v[204:207], v166 offset:53248
	ds_read_b128 v[208:211], v166 offset:54272
	ds_read_b128 v[212:215], v166 offset:55296
	ds_read_b128 v[216:219], v166 offset:56320
	ds_read_b128 v[220:223], v166 offset:57344
	ds_read_b128 v[240:243], v166 offset:58368
	ds_read_b128 v[244:247], v166 offset:59392
	ds_read_b128 v[248:251], v166 offset:60416
	global_load_lds_dwordx4 v[230:231], off
	v_lshl_add_u64 v[230:231], v[192:193], 0, s[4:5]
	s_add_i32 m0, s14, 0x2000
	s_add_i32 s14, s55, s17
	global_load_lds_dwordx4 v[230:231], off
	v_lshl_add_u64 v[230:231], v[192:193], 0, s[6:7]
	s_mov_b32 m0, s14
	v_lshl_add_u64 v[192:193], v[192:193], 0, s[8:9]
	global_load_lds_dwordx4 v[230:231], off
	s_add_i32 m0, s14, 0x2000
	v_lshl_add_u64 v[184:185], v[184:185], 0, s[92:93]
	global_load_lds_dwordx4 v[192:193], off
	v_lshl_add_u64 v[192:193], v[224:225], 0, s[92:93]
	s_mov_b32 m0, s80
	s_nop 0
	global_load_lds_dwordx4 v[192:193], off
	s_mov_b32 m0, s81
	s_nop 0
	global_load_lds_dwordx4 v[184:185], off
	s_waitcnt vmcnt(8)
	s_waitcnt lgkmcnt(0)
	s_barrier
	s_waitcnt lgkmcnt(0)
	v_mfma_f32_16x16x32_bf16 v[70:73], v[78:81], v[204:207], v[70:73]
	v_mfma_f32_16x16x32_bf16 v[54:57], v[158:161], v[204:207], v[54:57]
	s_add_i32 s34, s34, 2
	v_mfma_f32_16x16x32_bf16 v[46:49], v[78:81], v[212:215], v[46:49]
	s_add_u32 s40, s40, 0x100
	v_mfma_f32_16x16x32_bf16 v[38:41], v[158:161], v[212:215], v[38:41]
	s_addc_u32 s41, s41, 0
	v_mfma_f32_16x16x32_bf16 v[30:33], v[78:81], v[220:223], v[30:33]
	s_add_u32 s14, s70, s40
	v_mfma_f32_16x16x32_bf16 v[22:25], v[158:161], v[220:223], v[22:25]
	s_addc_u32 s15, s71, s41
	v_mfma_f32_16x16x32_bf16 v[14:17], v[78:81], v[244:247], v[14:17]
	s_add_u32 s35, s14, 0x100
	v_mfma_f32_16x16x32_bf16 v[6:9], v[158:161], v[244:247], v[6:9]
	s_addc_u32 s55, s15, 0
	v_mfma_f32_16x16x32_bf16 v[70:73], v[154:157], v[208:211], v[70:73]
	s_add_u32 s61, s1, s40
	v_mfma_f32_16x16x32_bf16 v[54:57], v[172:175], v[208:211], v[54:57]
	s_addc_u32 s69, s2, s41
	v_mfma_f32_16x16x32_bf16 v[46:49], v[154:157], v[216:219], v[46:49]
	s_cmpk_eq_i32 s40, 0x700
	v_mfma_f32_16x16x32_bf16 v[38:41], v[172:175], v[216:219], v[38:41]
	s_cselect_b64 vcc, -1, 0
	v_mfma_f32_16x16x32_bf16 v[30:33], v[154:157], v[240:243], v[30:33]
	s_and_b64 s[14:15], vcc, exec
	v_mfma_f32_16x16x32_bf16 v[22:25], v[172:175], v[240:243], v[22:25]
	s_cselect_b32 s15, s59, s55
	v_mfma_f32_16x16x32_bf16 v[14:17], v[154:157], v[248:251], v[14:17]
	s_cselect_b32 s14, s58, s35
	v_mfma_f32_16x16x32_bf16 v[6:9], v[172:175], v[248:251], v[6:9]
	s_cselect_b32 s73, s57, s69
	v_mfma_f32_16x16x32_bf16 v[66:69], v[176:179], v[204:207], v[66:69]
	s_cselect_b32 s72, s56, s61
	v_mfma_f32_16x16x32_bf16 v[50:53], v[196:199], v[204:207], v[50:53]
	s_add_i32 s35, 0, 0x11000
	v_mfma_f32_16x16x32_bf16 v[42:45], v[176:179], v[212:215], v[42:45]
	s_add_i32 s55, 0, 0x15000
	v_mfma_f32_16x16x32_bf16 v[34:37], v[196:199], v[212:215], v[34:37]
	v_mfma_f32_16x16x32_bf16 v[26:29], v[176:179], v[220:223], v[26:29]
	v_mfma_f32_16x16x32_bf16 v[18:21], v[196:199], v[220:223], v[18:21]
	v_mfma_f32_16x16x32_bf16 v[10:13], v[176:179], v[244:247], v[10:13]
	v_mfma_f32_16x16x32_bf16 v[2:5], v[196:199], v[244:247], v[2:5]
	v_mfma_f32_16x16x32_bf16 v[66:69], v[180:183], v[208:211], v[66:69]
	v_mfma_f32_16x16x32_bf16 v[50:53], v[200:203], v[208:211], v[50:53]
	v_mfma_f32_16x16x32_bf16 v[42:45], v[180:183], v[216:219], v[42:45]
	v_mfma_f32_16x16x32_bf16 v[34:37], v[200:203], v[216:219], v[34:37]
	v_mfma_f32_16x16x32_bf16 v[26:29], v[180:183], v[240:243], v[26:29]
	v_mfma_f32_16x16x32_bf16 v[18:21], v[200:203], v[240:243], v[18:21]
	v_mfma_f32_16x16x32_bf16 v[10:13], v[180:183], v[248:251], v[10:13]
	v_mfma_f32_16x16x32_bf16 v[2:5], v[200:203], v[248:251], v[2:5]
	s_barrier
	s_cmp_gt_u32 s34, 13
	s_cbranch_scc0 .LBB0_1339
	s_setprio 0
	s_lshl_b32 s1, s60, 8
	s_or_b32 s14, s1, s84
	s_ashr_i32 s15, s14, 31
	s_lshl_b64 s[14:15], s[14:15], 2
	s_add_u32 s1, s74, s14
	s_addc_u32 s2, s75, s15
	s_ashr_i32 s69, s68, 31
	s_lshl_b64 s[14:15], s[68:69], 13
	s_add_u32 s14, s1, s14
	s_addc_u32 s15, s2, s15
	v_lshl_add_u64 v[78:79], s[14:15], 0, v[150:151]
	global_load_dwordx4 v[58:61], v[78:79], off offset:48
	global_load_dwordx4 v[62:65], v[78:79], off offset:32
	global_load_dwordx4 v[74:77], v[78:79], off offset:16
	s_nop 0
	global_load_dwordx4 v[78:81], v[78:79], off
	s_and_b64 vcc, exec, s[50:51]
	s_cbranch_vccz .LBB0_1342
	s_barrier

.LBB0_1462:
	s_andn2_b64 vcc, exec, s[44:45]
	s_cbranch_vccnz .Lprio_dn
	s_setprio 1
.Lprio_dn:
	s_add_u32 s2, s56, 0x100
	s_addc_u32 s24, s57, 0
	s_add_u32 s56, s58, 0x40080
	s_waitcnt lgkmcnt(0)
	s_addc_u32 s57, s59, 0
	s_mov_b32 s25, -2
	s_add_u32 s14, s56, 0xfffc0080
	s_addc_u32 s15, s57, -1
	s_add_i32 s49, 0, 0x11000
	s_cmp_eq_u32 s25, 12
	s_cselect_b32 s15, s53, s15
	s_cselect_b32 s14, s52, s14
	v_add_u32_e32 v155, s49, v1
	s_cselect_b32 s35, s51, s24
	s_cselect_b32 s34, s50, s2
	s_add_i32 s55, 0, 0x15000
	ds_read_b128 v[156:159], v155
	ds_read_b128 v[160:163], v155 offset:1024
	ds_read_b128 v[164:167], v155 offset:2048
	ds_read_b128 v[168:171], v155 offset:3072
	v_add_u32_e32 v155, s55, v1
	ds_read_b128 v[172:175], v155
	ds_read_b128 v[176:179], v155 offset:1024
	ds_read_b128 v[180:183], v155 offset:2048
	ds_read_b128 v[196:199], v155 offset:3072
	v_lshl_add_u64 v[184:185], s[56:57], 0, v[152:153]
	s_add_i32 m0, s61, 0xd000
	ds_read_b128 v[200:203], v154 offset:4096
	ds_read_b128 v[204:207], v154 offset:5120
	ds_read_b128 v[208:211], v154 offset:6144
	ds_read_b128 v[212:215], v154 offset:7168
	ds_read_b128 v[216:219], v154 offset:8192
	ds_read_b128 v[220:223], v154 offset:9216
	ds_read_b128 v[240:243], v154 offset:10240
	ds_read_b128 v[244:247], v154 offset:11264
	global_load_lds_dwordx4 v[184:185], off
	v_lshl_add_u64 v[184:185], v[184:185], 0, s[82:83]
	s_add_i32 m0, s61, 0xf000
	s_nop 0
	global_load_lds_dwordx4 v[184:185], off
	s_waitcnt vmcnt(8)
	s_waitcnt lgkmcnt(0)
	s_barrier
	s_waitcnt lgkmcnt(0)
	v_mfma_f32_16x16x32_bf16 v[142:145], v[156:159], v[200:203], 0
	v_mfma_f32_16x16x32_bf16 v[138:141], v[164:167], v[200:203], 0
	v_mfma_f32_16x16x32_bf16 v[126:129], v[156:159], v[208:211], 0
	v_mfma_f32_16x16x32_bf16 v[122:125], v[164:167], v[208:211], 0
	v_mfma_f32_16x16x32_bf16 v[110:113], v[156:159], v[216:219], 0
	v_mfma_f32_16x16x32_bf16 v[106:109], v[164:167], v[216:219], 0
	v_mfma_f32_16x16x32_bf16 v[94:97], v[156:159], v[240:243], 0
	v_mfma_f32_16x16x32_bf16 v[90:93], v[164:167], v[240:243], 0
	v_mfma_f32_16x16x32_bf16 v[142:145], v[160:163], v[204:207], v[142:145]
	v_mfma_f32_16x16x32_bf16 v[138:141], v[168:171], v[204:207], v[138:141]
	v_mfma_f32_16x16x32_bf16 v[126:129], v[160:163], v[212:215], v[126:129]
	v_mfma_f32_16x16x32_bf16 v[122:125], v[168:171], v[212:215], v[122:125]
	v_mfma_f32_16x16x32_bf16 v[110:113], v[160:163], v[220:223], v[110:113]
	v_mfma_f32_16x16x32_bf16 v[106:109], v[168:171], v[220:223], v[106:109]
	v_mfma_f32_16x16x32_bf16 v[94:97], v[160:163], v[244:247], v[94:97]
	v_mfma_f32_16x16x32_bf16 v[90:93], v[168:171], v[244:247], v[90:93]
	v_mfma_f32_16x16x32_bf16 v[134:137], v[172:175], v[200:203], 0
	v_mfma_f32_16x16x32_bf16 v[130:133], v[180:183], v[200:203], 0
	v_mfma_f32_16x16x32_bf16 v[118:121], v[172:175], v[208:211], 0
	v_mfma_f32_16x16x32_bf16 v[114:117], v[180:183], v[208:211], 0
	v_mfma_f32_16x16x32_bf16 v[102:105], v[172:175], v[216:219], 0
	v_mfma_f32_16x16x32_bf16 v[98:101], v[180:183], v[216:219], 0
	v_mfma_f32_16x16x32_bf16 v[86:89], v[172:175], v[240:243], 0
	v_mfma_f32_16x16x32_bf16 v[82:85], v[180:183], v[240:243], 0
	v_mfma_f32_16x16x32_bf16 v[134:137], v[176:179], v[204:207], v[134:137]
	v_mfma_f32_16x16x32_bf16 v[130:133], v[196:199], v[204:207], v[130:133]
	v_mfma_f32_16x16x32_bf16 v[118:121], v[176:179], v[212:215], v[118:121]
	v_mfma_f32_16x16x32_bf16 v[114:117], v[196:199], v[212:215], v[114:117]
	v_mfma_f32_16x16x32_bf16 v[102:105], v[176:179], v[220:223], v[102:105]
	v_mfma_f32_16x16x32_bf16 v[98:101], v[196:199], v[220:223], v[98:101]
	v_mfma_f32_16x16x32_bf16 v[86:89], v[176:179], v[244:247], v[86:89]
	v_mfma_f32_16x16x32_bf16 v[82:85], v[196:199], v[244:247], v[82:85]
	s_barrier
	v_lshl_add_u64 v[184:185], s[34:35], 0, v[186:187]
	s_add_i32 s34, s49, s28
	s_mov_b32 m0, s34
	ds_read_b128 v[200:203], v154 offset:20480
	ds_read_b128 v[204:207], v154 offset:21504
	ds_read_b128 v[208:211], v154 offset:22528
	ds_read_b128 v[212:215], v154 offset:23552
	ds_read_b128 v[216:219], v154 offset:24576
	ds_read_b128 v[220:223], v154 offset:25600
	ds_read_b128 v[240:243], v154 offset:26624
	ds_read_b128 v[244:247], v154 offset:27648
	global_load_lds_dwordx4 v[184:185], off
	v_lshl_add_u64 v[192:193], v[184:185], 0, s[82:83]
	s_add_i32 m0, s34, 0x2000
	s_add_i32 s34, s55, s28
	global_load_lds_dwordx4 v[192:193], off
	v_lshl_add_u64 v[192:193], v[184:185], 0, s[64:65]
	s_mov_b32 m0, s34
	s_nop 0
	global_load_lds_dwordx4 v[192:193], off
	v_lshl_add_u64 v[192:193], v[184:185], 0, s[86:87]
	s_add_i32 m0, s34, 0x2000
	s_nop 0
	global_load_lds_dwordx4 v[192:193], off
	v_lshl_add_u64 v[192:193], s[14:15], 0, v[146:147]
	s_mov_b32 m0, s68
	v_lshl_add_u64 v[224:225], v[192:193], 0, s[82:83]
	global_load_lds_dwordx4 v[192:193], off
	s_mov_b32 m0, s69
	s_nop 0
	global_load_lds_dwordx4 v[224:225], off
	s_waitcnt vmcnt(8)
	s_waitcnt lgkmcnt(0)
	s_barrier
	s_waitcnt lgkmcnt(0)
	v_mfma_f32_16x16x32_bf16 v[78:81], v[156:159], v[200:203], 0
	v_mfma_f32_16x16x32_bf16 v[74:77], v[164:167], v[200:203], 0
	v_mfma_f32_16x16x32_bf16 v[62:65], v[156:159], v[208:211], 0
	v_mfma_f32_16x16x32_bf16 v[58:61], v[164:167], v[208:211], 0
	v_mfma_f32_16x16x32_bf16 v[46:49], v[156:159], v[216:219], 0
	v_mfma_f32_16x16x32_bf16 v[42:45], v[164:167], v[216:219], 0
	v_mfma_f32_16x16x32_bf16 v[30:33], v[156:159], v[240:243], 0
	v_mfma_f32_16x16x32_bf16 v[26:29], v[164:167], v[240:243], 0
	v_mfma_f32_16x16x32_bf16 v[78:81], v[160:163], v[204:207], v[78:81]
	v_mfma_f32_16x16x32_bf16 v[74:77], v[168:171], v[204:207], v[74:77]
	v_mfma_f32_16x16x32_bf16 v[62:65], v[160:163], v[212:215], v[62:65]
	v_mfma_f32_16x16x32_bf16 v[58:61], v[168:171], v[212:215], v[58:61]
	v_mfma_f32_16x16x32_bf16 v[46:49], v[160:163], v[220:223], v[46:49]
	v_mfma_f32_16x16x32_bf16 v[42:45], v[168:171], v[220:223], v[42:45]
	v_mfma_f32_16x16x32_bf16 v[30:33], v[160:163], v[244:247], v[30:33]
	v_mfma_f32_16x16x32_bf16 v[26:29], v[168:171], v[244:247], v[26:29]
	v_mfma_f32_16x16x32_bf16 v[70:73], v[172:175], v[200:203], 0
	v_mfma_f32_16x16x32_bf16 v[66:69], v[180:183], v[200:203], 0
	v_mfma_f32_16x16x32_bf16 v[54:57], v[172:175], v[208:211], 0
	v_mfma_f32_16x16x32_bf16 v[50:53], v[180:183], v[208:211], 0
	v_mfma_f32_16x16x32_bf16 v[38:41], v[172:175], v[216:219], 0
	v_mfma_f32_16x16x32_bf16 v[34:37], v[180:183], v[216:219], 0
	v_mfma_f32_16x16x32_bf16 v[22:25], v[172:175], v[240:243], 0
	v_mfma_f32_16x16x32_bf16 v[18:21], v[180:183], v[240:243], 0
	v_mfma_f32_16x16x32_bf16 v[70:73], v[176:179], v[204:207], v[70:73]
	v_mfma_f32_16x16x32_bf16 v[66:69], v[196:199], v[204:207], v[66:69]
	v_mfma_f32_16x16x32_bf16 v[54:57], v[176:179], v[212:215], v[54:57]
	v_mfma_f32_16x16x32_bf16 v[50:53], v[196:199], v[212:215], v[50:53]
	v_mfma_f32_16x16x32_bf16 v[38:41], v[176:179], v[220:223], v[38:41]
	v_mfma_f32_16x16x32_bf16 v[34:37], v[196:199], v[220:223], v[34:37]
	v_mfma_f32_16x16x32_bf16 v[22:25], v[176:179], v[244:247], v[22:25]
	v_mfma_f32_16x16x32_bf16 v[18:21], v[196:199], v[244:247], v[18:21]
	s_barrier
	s_add_i32 s14, 0, 0x19000
	v_add_u32_e32 v155, s14, v1
	s_add_i32 s15, 0, 0x1d000
	ds_read_b128 v[156:159], v155
	ds_read_b128 v[160:163], v155 offset:1024
	ds_read_b128 v[164:167], v155 offset:2048
	ds_read_b128 v[168:171], v155 offset:3072
	v_add_u32_e32 v155, s15, v1
	ds_read_b128 v[172:175], v155
	ds_read_b128 v[176:179], v155 offset:1024
	ds_read_b128 v[180:183], v155 offset:2048
	ds_read_b128 v[196:199], v155 offset:3072
	s_mov_b32 m0, s70
	v_lshl_add_u64 v[224:225], v[192:193], 0, s[64:65]
	ds_read_b128 v[200:203], v154 offset:36864
	ds_read_b128 v[204:207], v154 offset:37888
	ds_read_b128 v[208:211], v154 offset:38912
	ds_read_b128 v[212:215], v154 offset:39936
	ds_read_b128 v[216:219], v154 offset:40960
	ds_read_b128 v[220:223], v154 offset:41984
	ds_read_b128 v[240:243], v154 offset:43008
	ds_read_b128 v[244:247], v154 offset:44032
	global_load_lds_dwordx4 v[224:225], off
	v_lshl_add_u64 v[224:225], v[192:193], 0, s[86:87]
	s_mov_b32 m0, s71
	s_nop 0
	global_load_lds_dwordx4 v[224:225], off
	s_waitcnt vmcnt(8)
	s_waitcnt lgkmcnt(0)
	s_barrier
	s_waitcnt lgkmcnt(0)
	v_mfma_f32_16x16x32_bf16 v[142:145], v[156:159], v[200:203], v[142:145]
	v_mfma_f32_16x16x32_bf16 v[138:141], v[164:167], v[200:203], v[138:141]
	v_mfma_f32_16x16x32_bf16 v[126:129], v[156:159], v[208:211], v[126:129]
	v_mfma_f32_16x16x32_bf16 v[122:125], v[164:167], v[208:211], v[122:125]
	v_mfma_f32_16x16x32_bf16 v[110:113], v[156:159], v[216:219], v[110:113]
	v_mfma_f32_16x16x32_bf16 v[106:109], v[164:167], v[216:219], v[106:109]
	v_mfma_f32_16x16x32_bf16 v[94:97], v[156:159], v[240:243], v[94:97]
	v_mfma_f32_16x16x32_bf16 v[90:93], v[164:167], v[240:243], v[90:93]
	v_mfma_f32_16x16x32_bf16 v[142:145], v[160:163], v[204:207], v[142:145]
	v_mfma_f32_16x16x32_bf16 v[138:141], v[168:171], v[204:207], v[138:141]
	v_mfma_f32_16x16x32_bf16 v[126:129], v[160:163], v[212:215], v[126:129]
	v_mfma_f32_16x16x32_bf16 v[122:125], v[168:171], v[212:215], v[122:125]
	v_mfma_f32_16x16x32_bf16 v[110:113], v[160:163], v[220:223], v[110:113]
	v_mfma_f32_16x16x32_bf16 v[106:109], v[168:171], v[220:223], v[106:109]
	v_mfma_f32_16x16x32_bf16 v[94:97], v[160:163], v[244:247], v[94:97]
	v_mfma_f32_16x16x32_bf16 v[90:93], v[168:171], v[244:247], v[90:93]
	v_mfma_f32_16x16x32_bf16 v[134:137], v[172:175], v[200:203], v[134:137]
	v_mfma_f32_16x16x32_bf16 v[130:133], v[180:183], v[200:203], v[130:133]
	v_mfma_f32_16x16x32_bf16 v[118:121], v[172:175], v[208:211], v[118:121]
	v_mfma_f32_16x16x32_bf16 v[114:117], v[180:183], v[208:211], v[114:117]
	v_mfma_f32_16x16x32_bf16 v[102:105], v[172:175], v[216:219], v[102:105]
	v_mfma_f32_16x16x32_bf16 v[98:101], v[180:183], v[216:219], v[98:101]
	v_mfma_f32_16x16x32_bf16 v[86:89], v[172:175], v[240:243], v[86:89]
	v_mfma_f32_16x16x32_bf16 v[82:85], v[180:183], v[240:243], v[82:85]
	v_mfma_f32_16x16x32_bf16 v[134:137], v[176:179], v[204:207], v[134:137]
	v_mfma_f32_16x16x32_bf16 v[130:133], v[196:199], v[204:207], v[130:133]
	v_mfma_f32_16x16x32_bf16 v[118:121], v[176:179], v[212:215], v[118:121]
	v_mfma_f32_16x16x32_bf16 v[114:117], v[196:199], v[212:215], v[114:117]
	v_mfma_f32_16x16x32_bf16 v[102:105], v[176:179], v[220:223], v[102:105]
	v_mfma_f32_16x16x32_bf16 v[98:101], v[196:199], v[220:223], v[98:101]
	v_mfma_f32_16x16x32_bf16 v[86:89], v[176:179], v[244:247], v[86:89]
	v_mfma_f32_16x16x32_bf16 v[82:85], v[196:199], v[244:247], v[82:85]
	s_barrier
	s_add_i32 s14, s14, s28
	v_lshl_add_u64 v[224:225], v[184:185], 0, s[92:93]
	s_mov_b32 m0, s14
	ds_read_b128 v[200:203], v154 offset:53248
	ds_read_b128 v[204:207], v154 offset:54272
	ds_read_b128 v[208:211], v154 offset:55296
	ds_read_b128 v[212:215], v154 offset:56320
	ds_read_b128 v[216:219], v154 offset:57344
	ds_read_b128 v[220:223], v154 offset:58368
	ds_read_b128 v[240:243], v154 offset:59392
	ds_read_b128 v[244:247], v154 offset:60416
	global_load_lds_dwordx4 v[224:225], off
	v_lshl_add_u64 v[224:225], v[184:185], 0, s[4:5]
	s_add_i32 m0, s14, 0x2000
	s_add_i32 s14, s15, s28
	global_load_lds_dwordx4 v[224:225], off
	v_lshl_add_u64 v[224:225], v[184:185], 0, s[6:7]
	s_mov_b32 m0, s14
	v_lshl_add_u64 v[184:185], v[184:185], 0, s[8:9]
	global_load_lds_dwordx4 v[224:225], off
	s_add_i32 m0, s14, 0x2000
	s_nop 0
	global_load_lds_dwordx4 v[184:185], off
	v_lshl_add_u64 v[184:185], v[192:193], 0, s[92:93]
	s_mov_b32 m0, s75
	s_nop 0
	global_load_lds_dwordx4 v[184:185], off
	v_lshl_add_u64 v[184:185], v[192:193], 0, s[4:5]
	s_mov_b32 m0, s76
	s_nop 0
	global_load_lds_dwordx4 v[184:185], off
	s_waitcnt vmcnt(8)
	s_waitcnt lgkmcnt(0)
	s_barrier
	s_waitcnt lgkmcnt(0)
	v_mfma_f32_16x16x32_bf16 v[78:81], v[156:159], v[200:203], v[78:81]
	v_mfma_f32_16x16x32_bf16 v[74:77], v[164:167], v[200:203], v[74:77]
	s_add_i32 s25, s25, 2
	v_mfma_f32_16x16x32_bf16 v[62:65], v[156:159], v[208:211], v[62:65]
	s_add_u32 s2, s2, 0x100
	v_mfma_f32_16x16x32_bf16 v[58:61], v[164:167], v[208:211], v[58:61]
	s_addc_u32 s24, s24, 0
	v_mfma_f32_16x16x32_bf16 v[46:49], v[156:159], v[216:219], v[46:49]
	s_add_u32 s56, s56, 0x100
	v_mfma_f32_16x16x32_bf16 v[42:45], v[164:167], v[216:219], v[42:45]
	s_addc_u32 s57, s57, 0
	v_mfma_f32_16x16x32_bf16 v[30:33], v[156:159], v[240:243], v[30:33]
	s_add_u32 s14, s56, 0xfffc0080
	v_mfma_f32_16x16x32_bf16 v[26:29], v[164:167], v[240:243], v[26:29]
	s_addc_u32 s15, s57, -1
	v_mfma_f32_16x16x32_bf16 v[78:81], v[160:163], v[204:207], v[78:81]
	s_add_i32 s49, 0, 0x11000
	v_mfma_f32_16x16x32_bf16 v[74:77], v[168:171], v[204:207], v[74:77]
	s_cmp_eq_u32 s25, 12
	v_mfma_f32_16x16x32_bf16 v[62:65], v[160:163], v[212:215], v[62:65]
	s_cselect_b32 s15, s53, s15
	v_mfma_f32_16x16x32_bf16 v[58:61], v[168:171], v[212:215], v[58:61]
	s_cselect_b32 s14, s52, s14
	v_mfma_f32_16x16x32_bf16 v[46:49], v[160:163], v[220:223], v[46:49]
	s_cselect_b32 s35, s51, s24
	v_mfma_f32_16x16x32_bf16 v[42:45], v[168:171], v[220:223], v[42:45]
	s_cselect_b32 s34, s50, s2
	v_mfma_f32_16x16x32_bf16 v[30:33], v[160:163], v[244:247], v[30:33]
	s_add_i32 s55, 0, 0x15000
	v_mfma_f32_16x16x32_bf16 v[26:29], v[168:171], v[244:247], v[26:29]
	v_mfma_f32_16x16x32_bf16 v[70:73], v[172:175], v[200:203], v[70:73]
	v_mfma_f32_16x16x32_bf16 v[66:69], v[180:183], v[200:203], v[66:69]
	v_mfma_f32_16x16x32_bf16 v[54:57], v[172:175], v[208:211], v[54:57]
	v_mfma_f32_16x16x32_bf16 v[50:53], v[180:183], v[208:211], v[50:53]
	v_mfma_f32_16x16x32_bf16 v[38:41], v[172:175], v[216:219], v[38:41]
	v_mfma_f32_16x16x32_bf16 v[34:37], v[180:183], v[216:219], v[34:37]
	v_mfma_f32_16x16x32_bf16 v[22:25], v[172:175], v[240:243], v[22:25]
	v_mfma_f32_16x16x32_bf16 v[18:21], v[180:183], v[240:243], v[18:21]
	v_mfma_f32_16x16x32_bf16 v[70:73], v[176:179], v[204:207], v[70:73]
	v_mfma_f32_16x16x32_bf16 v[66:69], v[196:199], v[204:207], v[66:69]
	v_mfma_f32_16x16x32_bf16 v[54:57], v[176:179], v[212:215], v[54:57]
	v_mfma_f32_16x16x32_bf16 v[50:53], v[196:199], v[212:215], v[50:53]
	v_mfma_f32_16x16x32_bf16 v[38:41], v[176:179], v[220:223], v[38:41]
	v_mfma_f32_16x16x32_bf16 v[34:37], v[196:199], v[220:223], v[34:37]
	v_mfma_f32_16x16x32_bf16 v[22:25], v[176:179], v[244:247], v[22:25]
	v_mfma_f32_16x16x32_bf16 v[18:21], v[196:199], v[244:247], v[18:21]
	s_barrier
.LBB0_1463:
	v_add_u32_e32 v155, s49, v1
	ds_read_b128 v[156:159], v155
	ds_read_b128 v[160:163], v155 offset:1024
	ds_read_b128 v[164:167], v155 offset:2048
	ds_read_b128 v[168:171], v155 offset:3072
	v_add_u32_e32 v155, s55, v1
	ds_read_b128 v[172:175], v155
	ds_read_b128 v[176:179], v155 offset:1024
	ds_read_b128 v[180:183], v155 offset:2048
	ds_read_b128 v[196:199], v155 offset:3072
	v_lshl_add_u64 v[184:185], s[56:57], 0, v[152:153]
	s_add_i32 m0, s61, 0xd000
	ds_read_b128 v[200:203], v154 offset:4096
	ds_read_b128 v[204:207], v154 offset:5120
	ds_read_b128 v[208:211], v154 offset:6144
	ds_read_b128 v[212:215], v154 offset:7168
	ds_read_b128 v[216:219], v154 offset:8192
	ds_read_b128 v[220:223], v154 offset:9216
	ds_read_b128 v[240:243], v154 offset:10240
	ds_read_b128 v[244:247], v154 offset:11264
	global_load_lds_dwordx4 v[184:185], off
	v_lshl_add_u64 v[184:185], v[184:185], 0, s[82:83]
	s_add_i32 m0, s61, 0xf000
	s_nop 0
	global_load_lds_dwordx4 v[184:185], off
	s_waitcnt vmcnt(8)
	s_waitcnt lgkmcnt(0)
	s_barrier
	s_waitcnt lgkmcnt(0)
	v_mfma_f32_16x16x32_bf16 v[142:145], v[156:159], v[200:203], v[142:145]
	v_mfma_f32_16x16x32_bf16 v[138:141], v[164:167], v[200:203], v[138:141]
	v_mfma_f32_16x16x32_bf16 v[126:129], v[156:159], v[208:211], v[126:129]
	v_mfma_f32_16x16x32_bf16 v[122:125], v[164:167], v[208:211], v[122:125]
	v_mfma_f32_16x16x32_bf16 v[110:113], v[156:159], v[216:219], v[110:113]
	v_mfma_f32_16x16x32_bf16 v[106:109], v[164:167], v[216:219], v[106:109]
	v_mfma_f32_16x16x32_bf16 v[94:97], v[156:159], v[240:243], v[94:97]
	v_mfma_f32_16x16x32_bf16 v[90:93], v[164:167], v[240:243], v[90:93]
	v_mfma_f32_16x16x32_bf16 v[142:145], v[160:163], v[204:207], v[142:145]
	v_mfma_f32_16x16x32_bf16 v[138:141], v[168:171], v[204:207], v[138:141]
	v_mfma_f32_16x16x32_bf16 v[126:129], v[160:163], v[212:215], v[126:129]
	v_mfma_f32_16x16x32_bf16 v[122:125], v[168:171], v[212:215], v[122:125]
	v_mfma_f32_16x16x32_bf16 v[110:113], v[160:163], v[220:223], v[110:113]
	v_mfma_f32_16x16x32_bf16 v[106:109], v[168:171], v[220:223], v[106:109]
	v_mfma_f32_16x16x32_bf16 v[94:97], v[160:163], v[244:247], v[94:97]
	v_mfma_f32_16x16x32_bf16 v[90:93], v[168:171], v[244:247], v[90:93]
	v_mfma_f32_16x16x32_bf16 v[134:137], v[172:175], v[200:203], v[134:137]
	v_mfma_f32_16x16x32_bf16 v[130:133], v[180:183], v[200:203], v[130:133]
	v_mfma_f32_16x16x32_bf16 v[118:121], v[172:175], v[208:211], v[118:121]
	v_mfma_f32_16x16x32_bf16 v[114:117], v[180:183], v[208:211], v[114:117]
	v_mfma_f32_16x16x32_bf16 v[102:105], v[172:175], v[216:219], v[102:105]
	v_mfma_f32_16x16x32_bf16 v[98:101], v[180:183], v[216:219], v[98:101]
	v_mfma_f32_16x16x32_bf16 v[86:89], v[172:175], v[240:243], v[86:89]
	v_mfma_f32_16x16x32_bf16 v[82:85], v[180:183], v[240:243], v[82:85]
	v_mfma_f32_16x16x32_bf16 v[134:137], v[176:179], v[204:207], v[134:137]
	v_mfma_f32_16x16x32_bf16 v[130:133], v[196:199], v[204:207], v[130:133]
	v_mfma_f32_16x16x32_bf16 v[118:121], v[176:179], v[212:215], v[118:121]
	v_mfma_f32_16x16x32_bf16 v[114:117], v[196:199], v[212:215], v[114:117]
	v_mfma_f32_16x16x32_bf16 v[102:105], v[176:179], v[220:223], v[102:105]
	v_mfma_f32_16x16x32_bf16 v[98:101], v[196:199], v[220:223], v[98:101]
	v_mfma_f32_16x16x32_bf16 v[86:89], v[176:179], v[244:247], v[86:89]
	v_mfma_f32_16x16x32_bf16 v[82:85], v[196:199], v[244:247], v[82:85]
	s_barrier
	v_lshl_add_u64 v[184:185], s[34:35], 0, v[186:187]
	s_add_i32 s34, s49, s28
	s_mov_b32 m0, s34
	ds_read_b128 v[200:203], v154 offset:20480
	ds_read_b128 v[204:207], v154 offset:21504
	ds_read_b128 v[208:211], v154 offset:22528
	ds_read_b128 v[212:215], v154 offset:23552
	ds_read_b128 v[216:219], v154 offset:24576
	ds_read_b128 v[220:223], v154 offset:25600
	ds_read_b128 v[240:243], v154 offset:26624
	ds_read_b128 v[244:247], v154 offset:27648
	global_load_lds_dwordx4 v[184:185], off
	v_lshl_add_u64 v[192:193], v[184:185], 0, s[82:83]
	s_add_i32 m0, s34, 0x2000
	s_add_i32 s34, s55, s28
	global_load_lds_dwordx4 v[192:193], off
	v_lshl_add_u64 v[192:193], v[184:185], 0, s[64:65]
	s_mov_b32 m0, s34
	s_nop 0
	global_load_lds_dwordx4 v[192:193], off
	v_lshl_add_u64 v[192:193], v[184:185], 0, s[86:87]
	s_add_i32 m0, s34, 0x2000
	s_nop 0
	global_load_lds_dwordx4 v[192:193], off
	v_lshl_add_u64 v[192:193], s[14:15], 0, v[146:147]
	s_mov_b32 m0, s68
	v_lshl_add_u64 v[224:225], v[192:193], 0, s[82:83]
	global_load_lds_dwordx4 v[192:193], off
	s_mov_b32 m0, s69
	s_nop 0
	global_load_lds_dwordx4 v[224:225], off
	s_waitcnt vmcnt(8)
	s_waitcnt lgkmcnt(0)
	s_barrier
	s_waitcnt lgkmcnt(0)
	v_mfma_f32_16x16x32_bf16 v[78:81], v[156:159], v[200:203], v[78:81]
	v_mfma_f32_16x16x32_bf16 v[74:77], v[164:167], v[200:203], v[74:77]
	v_mfma_f32_16x16x32_bf16 v[62:65], v[156:159], v[208:211], v[62:65]
	v_mfma_f32_16x16x32_bf16 v[58:61], v[164:167], v[208:211], v[58:61]
	v_mfma_f32_16x16x32_bf16 v[46:49], v[156:159], v[216:219], v[46:49]
	v_mfma_f32_16x16x32_bf16 v[42:45], v[164:167], v[216:219], v[42:45]
	v_mfma_f32_16x16x32_bf16 v[30:33], v[156:159], v[240:243], v[30:33]
	v_mfma_f32_16x16x32_bf16 v[26:29], v[164:167], v[240:243], v[26:29]
	v_mfma_f32_16x16x32_bf16 v[78:81], v[160:163], v[204:207], v[78:81]
	v_mfma_f32_16x16x32_bf16 v[74:77], v[168:171], v[204:207], v[74:77]
	v_mfma_f32_16x16x32_bf16 v[62:65], v[160:163], v[212:215], v[62:65]
	v_mfma_f32_16x16x32_bf16 v[58:61], v[168:171], v[212:215], v[58:61]
	v_mfma_f32_16x16x32_bf16 v[46:49], v[160:163], v[220:223], v[46:49]
	v_mfma_f32_16x16x32_bf16 v[42:45], v[168:171], v[220:223], v[42:45]
	v_mfma_f32_16x16x32_bf16 v[30:33], v[160:163], v[244:247], v[30:33]
	v_mfma_f32_16x16x32_bf16 v[26:29], v[168:171], v[244:247], v[26:29]
	v_mfma_f32_16x16x32_bf16 v[70:73], v[172:175], v[200:203], v[70:73]
	v_mfma_f32_16x16x32_bf16 v[66:69], v[180:183], v[200:203], v[66:69]
	v_mfma_f32_16x16x32_bf16 v[54:57], v[172:175], v[208:211], v[54:57]
	v_mfma_f32_16x16x32_bf16 v[50:53], v[180:183], v[208:211], v[50:53]
	v_mfma_f32_16x16x32_bf16 v[38:41], v[172:175], v[216:219], v[38:41]
	v_mfma_f32_16x16x32_bf16 v[34:37], v[180:183], v[216:219], v[34:37]
	v_mfma_f32_16x16x32_bf16 v[22:25], v[172:175], v[240:243], v[22:25]
	v_mfma_f32_16x16x32_bf16 v[18:21], v[180:183], v[240:243], v[18:21]
	v_mfma_f32_16x16x32_bf16 v[70:73], v[176:179], v[204:207], v[70:73]
	v_mfma_f32_16x16x32_bf16 v[66:69], v[196:199], v[204:207], v[66:69]
	v_mfma_f32_16x16x32_bf16 v[54:57], v[176:179], v[212:215], v[54:57]
	v_mfma_f32_16x16x32_bf16 v[50:53], v[196:199], v[212:215], v[50:53]
	v_mfma_f32_16x16x32_bf16 v[38:41], v[176:179], v[220:223], v[38:41]
	v_mfma_f32_16x16x32_bf16 v[34:37], v[196:199], v[220:223], v[34:37]
	v_mfma_f32_16x16x32_bf16 v[22:25], v[176:179], v[244:247], v[22:25]
	v_mfma_f32_16x16x32_bf16 v[18:21], v[196:199], v[244:247], v[18:21]
	s_barrier
	s_add_i32 s14, 0, 0x19000
	v_add_u32_e32 v155, s14, v1
	s_add_i32 s15, 0, 0x1d000
	ds_read_b128 v[156:159], v155
	ds_read_b128 v[160:163], v155 offset:1024
	ds_read_b128 v[164:167], v155 offset:2048
	ds_read_b128 v[168:171], v155 offset:3072
	v_add_u32_e32 v155, s15, v1
	ds_read_b128 v[172:175], v155
	ds_read_b128 v[176:179], v155 offset:1024
	ds_read_b128 v[180:183], v155 offset:2048
	ds_read_b128 v[196:199], v155 offset:3072
	s_mov_b32 m0, s70
	v_lshl_add_u64 v[224:225], v[192:193], 0, s[64:65]
	ds_read_b128 v[200:203], v154 offset:36864
	ds_read_b128 v[204:207], v154 offset:37888
	ds_read_b128 v[208:211], v154 offset:38912
	ds_read_b128 v[212:215], v154 offset:39936
	ds_read_b128 v[216:219], v154 offset:40960
	ds_read_b128 v[220:223], v154 offset:41984
	ds_read_b128 v[240:243], v154 offset:43008
	ds_read_b128 v[244:247], v154 offset:44032
	global_load_lds_dwordx4 v[224:225], off
	v_lshl_add_u64 v[224:225], v[192:193], 0, s[86:87]
	s_mov_b32 m0, s71
	s_nop 0
	global_load_lds_dwordx4 v[224:225], off
	s_waitcnt vmcnt(8)
	s_waitcnt lgkmcnt(0)
	s_barrier
	s_waitcnt lgkmcnt(0)
	v_mfma_f32_16x16x32_bf16 v[142:145], v[156:159], v[200:203], v[142:145]
	v_mfma_f32_16x16x32_bf16 v[138:141], v[164:167], v[200:203], v[138:141]
	v_mfma_f32_16x16x32_bf16 v[126:129], v[156:159], v[208:211], v[126:129]
	v_mfma_f32_16x16x32_bf16 v[122:125], v[164:167], v[208:211], v[122:125]
	v_mfma_f32_16x16x32_bf16 v[110:113], v[156:159], v[216:219], v[110:113]
	v_mfma_f32_16x16x32_bf16 v[106:109], v[164:167], v[216:219], v[106:109]
	v_mfma_f32_16x16x32_bf16 v[94:97], v[156:159], v[240:243], v[94:97]
	v_mfma_f32_16x16x32_bf16 v[90:93], v[164:167], v[240:243], v[90:93]
	v_mfma_f32_16x16x32_bf16 v[142:145], v[160:163], v[204:207], v[142:145]
	v_mfma_f32_16x16x32_bf16 v[138:141], v[168:171], v[204:207], v[138:141]
	v_mfma_f32_16x16x32_bf16 v[126:129], v[160:163], v[212:215], v[126:129]
	v_mfma_f32_16x16x32_bf16 v[122:125], v[168:171], v[212:215], v[122:125]
	v_mfma_f32_16x16x32_bf16 v[110:113], v[160:163], v[220:223], v[110:113]
	v_mfma_f32_16x16x32_bf16 v[106:109], v[168:171], v[220:223], v[106:109]
	v_mfma_f32_16x16x32_bf16 v[94:97], v[160:163], v[244:247], v[94:97]
	v_mfma_f32_16x16x32_bf16 v[90:93], v[168:171], v[244:247], v[90:93]
	v_mfma_f32_16x16x32_bf16 v[134:137], v[172:175], v[200:203], v[134:137]
	v_mfma_f32_16x16x32_bf16 v[130:133], v[180:183], v[200:203], v[130:133]
	v_mfma_f32_16x16x32_bf16 v[118:121], v[172:175], v[208:211], v[118:121]
	v_mfma_f32_16x16x32_bf16 v[114:117], v[180:183], v[208:211], v[114:117]
	v_mfma_f32_16x16x32_bf16 v[102:105], v[172:175], v[216:219], v[102:105]
	v_mfma_f32_16x16x32_bf16 v[98:101], v[180:183], v[216:219], v[98:101]
	v_mfma_f32_16x16x32_bf16 v[86:89], v[172:175], v[240:243], v[86:89]
	v_mfma_f32_16x16x32_bf16 v[82:85], v[180:183], v[240:243], v[82:85]
	v_mfma_f32_16x16x32_bf16 v[134:137], v[176:179], v[204:207], v[134:137]
	v_mfma_f32_16x16x32_bf16 v[130:133], v[196:199], v[204:207], v[130:133]
	v_mfma_f32_16x16x32_bf16 v[118:121], v[176:179], v[212:215], v[118:121]
	v_mfma_f32_16x16x32_bf16 v[114:117], v[196:199], v[212:215], v[114:117]
	v_mfma_f32_16x16x32_bf16 v[102:105], v[176:179], v[220:223], v[102:105]
	v_mfma_f32_16x16x32_bf16 v[98:101], v[196:199], v[220:223], v[98:101]
	v_mfma_f32_16x16x32_bf16 v[86:89], v[176:179], v[244:247], v[86:89]
	v_mfma_f32_16x16x32_bf16 v[82:85], v[196:199], v[244:247], v[82:85]
	s_barrier
	s_add_i32 s14, s14, s28
	v_lshl_add_u64 v[224:225], v[184:185], 0, s[92:93]
	s_mov_b32 m0, s14
	ds_read_b128 v[200:203], v154 offset:53248
	ds_read_b128 v[204:207], v154 offset:54272
	ds_read_b128 v[208:211], v154 offset:55296
	ds_read_b128 v[212:215], v154 offset:56320
	ds_read_b128 v[216:219], v154 offset:57344
	ds_read_b128 v[220:223], v154 offset:58368
	ds_read_b128 v[240:243], v154 offset:59392
	ds_read_b128 v[244:247], v154 offset:60416
	global_load_lds_dwordx4 v[224:225], off
	v_lshl_add_u64 v[224:225], v[184:185], 0, s[4:5]
	s_add_i32 m0, s14, 0x2000
	s_add_i32 s14, s15, s28
	global_load_lds_dwordx4 v[224:225], off
	v_lshl_add_u64 v[224:225], v[184:185], 0, s[6:7]
	s_mov_b32 m0, s14
	v_lshl_add_u64 v[184:185], v[184:185], 0, s[8:9]
	global_load_lds_dwordx4 v[224:225], off
	s_add_i32 m0, s14, 0x2000
	s_nop 0
	global_load_lds_dwordx4 v[184:185], off
	v_lshl_add_u64 v[184:185], v[192:193], 0, s[92:93]
	s_mov_b32 m0, s75
	s_nop 0
	global_load_lds_dwordx4 v[184:185], off
	v_lshl_add_u64 v[184:185], v[192:193], 0, s[4:5]
	s_mov_b32 m0, s76
	s_nop 0
	global_load_lds_dwordx4 v[184:185], off
	s_waitcnt vmcnt(8)
	s_waitcnt lgkmcnt(0)
	s_barrier
	s_waitcnt lgkmcnt(0)
	v_mfma_f32_16x16x32_bf16 v[78:81], v[156:159], v[200:203], v[78:81]
	v_mfma_f32_16x16x32_bf16 v[74:77], v[164:167], v[200:203], v[74:77]
	s_add_i32 s25, s25, 2
	v_mfma_f32_16x16x32_bf16 v[62:65], v[156:159], v[208:211], v[62:65]
	s_add_u32 s2, s2, 0x100
	v_mfma_f32_16x16x32_bf16 v[58:61], v[164:167], v[208:211], v[58:61]
	s_addc_u32 s24, s24, 0
	v_mfma_f32_16x16x32_bf16 v[46:49], v[156:159], v[216:219], v[46:49]
	s_add_u32 s56, s56, 0x100
	v_mfma_f32_16x16x32_bf16 v[42:45], v[164:167], v[216:219], v[42:45]
	s_addc_u32 s57, s57, 0
	v_mfma_f32_16x16x32_bf16 v[30:33], v[156:159], v[240:243], v[30:33]
	s_add_u32 s14, s56, 0xfffc0080
	v_mfma_f32_16x16x32_bf16 v[26:29], v[164:167], v[240:243], v[26:29]
	s_addc_u32 s15, s57, -1
	v_mfma_f32_16x16x32_bf16 v[78:81], v[160:163], v[204:207], v[78:81]
	s_add_i32 s49, 0, 0x11000
	v_mfma_f32_16x16x32_bf16 v[74:77], v[168:171], v[204:207], v[74:77]
	s_cmp_eq_u32 s25, 12
	v_mfma_f32_16x16x32_bf16 v[62:65], v[160:163], v[212:215], v[62:65]
	s_cselect_b32 s15, s53, s15
	v_mfma_f32_16x16x32_bf16 v[58:61], v[168:171], v[212:215], v[58:61]
	s_cselect_b32 s14, s52, s14
	v_mfma_f32_16x16x32_bf16 v[46:49], v[160:163], v[220:223], v[46:49]
	s_cselect_b32 s35, s51, s24
	v_mfma_f32_16x16x32_bf16 v[42:45], v[168:171], v[220:223], v[42:45]
	s_cselect_b32 s34, s50, s2
	v_mfma_f32_16x16x32_bf16 v[30:33], v[160:163], v[244:247], v[30:33]
	s_add_i32 s55, 0, 0x15000
	v_mfma_f32_16x16x32_bf16 v[26:29], v[168:171], v[244:247], v[26:29]
	v_mfma_f32_16x16x32_bf16 v[70:73], v[172:175], v[200:203], v[70:73]
	v_mfma_f32_16x16x32_bf16 v[66:69], v[180:183], v[200:203], v[66:69]
	v_mfma_f32_16x16x32_bf16 v[54:57], v[172:175], v[208:211], v[54:57]
	v_mfma_f32_16x16x32_bf16 v[50:53], v[180:183], v[208:211], v[50:53]
	v_mfma_f32_16x16x32_bf16 v[38:41], v[172:175], v[216:219], v[38:41]
	v_mfma_f32_16x16x32_bf16 v[34:37], v[180:183], v[216:219], v[34:37]
	v_mfma_f32_16x16x32_bf16 v[22:25], v[172:175], v[240:243], v[22:25]
	v_mfma_f32_16x16x32_bf16 v[18:21], v[180:183], v[240:243], v[18:21]
	v_mfma_f32_16x16x32_bf16 v[70:73], v[176:179], v[204:207], v[70:73]
	v_mfma_f32_16x16x32_bf16 v[66:69], v[196:199], v[204:207], v[66:69]
	v_mfma_f32_16x16x32_bf16 v[54:57], v[176:179], v[212:215], v[54:57]
	v_mfma_f32_16x16x32_bf16 v[50:53], v[196:199], v[212:215], v[50:53]
	v_mfma_f32_16x16x32_bf16 v[38:41], v[176:179], v[220:223], v[38:41]
	v_mfma_f32_16x16x32_bf16 v[34:37], v[196:199], v[220:223], v[34:37]
	v_mfma_f32_16x16x32_bf16 v[22:25], v[176:179], v[244:247], v[22:25]
	v_mfma_f32_16x16x32_bf16 v[18:21], v[196:199], v[244:247], v[18:21]
	s_barrier
	s_cmp_gt_u32 s25, 13
	s_cbranch_scc0 .LBB0_1463
	s_setprio 0
	s_and_b64 vcc, exec, s[46:47]
	s_cbranch_vccz .LBB0_1466
	s_barrier
